# baseline (speedup 1.0000x reference)
_Z11pwconv_mfmaPKfPK15HIP_vector_typeIjLj4EES0_Pf:
	s_load_dwordx4 s[12:15], s[0:1], 0x0
	s_load_dwordx4 s[16:19], s[0:1], 0x10
	s_and_b32 s20, s2, 7
	s_lshr_b32 s21, s2, 3
	s_lshr_b32 s37, s20, 1
	s_and_b32 s36, s20, 1
	s_mul_i32 s36, s36, 31
	s_add_i32 s36, s36, s21
	s_lshr_b32 s21, s36, 1
	s_and_b32 s36, s36, 1
	s_lshl_b32 s37, s37, 1
	s_add_i32 s20, s37, s36
	v_lshrrev_b32_e32 v1, 6, v0
	v_and_b32_e32 v2, 63, v0
	s_nop 0
	v_readfirstlane_b32 s22, v1
	s_nop 3
	s_lshl_b32 s23, s20, 3
	s_add_i32 s23, s23, s22
	s_mul_i32 s24, s23, 0x439200
	s_mul_i32 s25, s21, 0x1f0
	s_add_u32 s24, s24, s25
	s_lshl_b32 s25, s21, 17
	s_lshl_b32 s26, s22, 13
	s_add_u32 s25, s25, s26
	s_mul_i32 s27, s20, 0x1e080
	s_mul_i32 s36, s21, 0x1f0
	s_add_u32 s27, s27, s36
	v_min_u32_e32 v10, 61, v2
	v_lshlrev_b32_e32 v3, 3, v10
	v_lshlrev_b32_e32 v4, 4, v2
	v_cmp_lt_u32_e32 vcc, 30, v10
	s_nop 1
	v_cndmask_b32_e64 v5, 0, 1, vcc
	v_mul_u32_u24_e32 v6, 31, v5
	v_sub_u32_e32 v6, v10, v6
	v_lshl_add_u32 v7, v1, 1, v5
	v_and_b32_e32 v8, 7, v6
	v_xor_b32_e32 v7, v7, v8
	v_lshlrev_b32_e32 v7, 4, v7
	v_lshl_add_u32 v5, v6, 12, v7
	s_lshl_b32 s36, s22, 2
	s_add_i32 s36, s36, 0
	s_and_b32 s36, s36, 7
	s_lshl_b32 s37, s22, 14
	s_add_i32 s37, s37, 0x0
	v_xor_b32_e32 v6, s36, v2
	v_lshlrev_b32_e32 v6, 4, v6
	v_add_u32_e32 v6, s37, v6
	s_lshl_b32 s36, s22, 2
	s_add_i32 s36, s36, 1
	s_and_b32 s36, s36, 7
	s_lshl_b32 s37, s22, 14
	s_add_i32 s37, s37, 0x1000
	v_xor_b32_e32 v7, s36, v2
	v_lshlrev_b32_e32 v7, 4, v7
	v_add_u32_e32 v7, s37, v7
	s_lshl_b32 s36, s22, 2
	s_add_i32 s36, s36, 2
	s_and_b32 s36, s36, 7
	s_lshl_b32 s37, s22, 14
	s_add_i32 s37, s37, 0x2000
	v_xor_b32_e32 v8, s36, v2
	v_lshlrev_b32_e32 v8, 4, v8
	v_add_u32_e32 v8, s37, v8
	s_lshl_b32 s36, s22, 2
	s_add_i32 s36, s36, 3
	s_and_b32 s36, s36, 7
	s_lshl_b32 s37, s22, 14
	s_add_i32 s37, s37, 0x3000
	v_xor_b32_e32 v9, s36, v2
	v_lshlrev_b32_e32 v9, 4, v9
	v_add_u32_e32 v9, s37, v9
	s_lshl_b32 s36, s22, 11
	s_add_i32 s36, s36, 0x20000
	v_add_u32_e32 v254, s36, v4
	s_add_i32 s37, s22, 1
	s_min_u32 s37, s37, 7
	s_lshl_b32 s37, s37, 11
	s_add_i32 s37, s37, 0x20000
	v_add_u32_e32 v255, s37, v4
	v_lshrrev_b32_e32 v10, 5, v0
	v_and_b32_e32 v11, 7, v10
	v_mul_u32_u24_e32 v11, 0x3c10, v11
	v_lshrrev_b32_e32 v10, 8, v0
	v_mul_u32_u24_e32 v10, 0xf0400, v10
	v_add_u32_e32 v11, v11, v10
	v_and_b32_e32 v10, 31, v0
	v_lshl_add_u32 v11, v10, 4, v11
	v_add_u32_e32 v11, s27, v11
	v_cmp_eq_u32_e32 vcc, 31, v10
	v_mov_b32_e32 v10, 0x7f000000
	s_nop 1
	v_cndmask_b32_e32 v11, v11, v10, vcc
	s_waitcnt lgkmcnt(0)
	s_add_u32 s4, s12, s24
	s_addc_u32 s5, s13, 0
	s_and_b32 s5, s5, 0xffff
	s_sub_u32 s6, 0x10e48000, s24
	s_mov_b32 s7, 0x20000
	s_add_u32 s8, s14, s25
	s_addc_u32 s9, s15, 0
	s_and_b32 s9, s9, 0xffff
	s_sub_u32 s10, 0x400000, s25
	s_mov_b32 s11, 0x20000
	s_mov_b32 s28, s16
	s_and_b32 s29, s17, 0xffff
	s_mov_b32 s30, 0xf0400
	s_mov_b32 s31, 0x20000
	s_mov_b32 s32, s18
	s_and_b32 s33, s19, 0xffff
	s_mov_b32 s34, 0xf04000
	s_mov_b32 s35, 0x20000
	s_mov_b32 s40, 0x0
	s_mov_b32 s41, 0x21c90
	s_mov_b32 s42, 0x43920
	s_mov_b32 s43, 0x655b0
	s_mov_b32 s44, 0x87240
	s_mov_b32 s45, 0xa8ed0
	s_mov_b32 s46, 0xcab60
	s_mov_b32 s47, 0xec7f0
	buffer_load_dwordx2 v[44:45], v3, s[4:7], s40 offen nt
	buffer_load_dwordx2 v[46:47], v3, s[4:7], s41 offen nt
	buffer_load_dwordx2 v[48:49], v3, s[4:7], s42 offen nt
	buffer_load_dwordx2 v[50:51], v3, s[4:7], s43 offen nt
	buffer_load_dwordx2 v[52:53], v3, s[4:7], s44 offen nt
	buffer_load_dwordx2 v[54:55], v3, s[4:7], s45 offen nt
	buffer_load_dwordx2 v[56:57], v3, s[4:7], s46 offen nt
	buffer_load_dwordx2 v[58:59], v3, s[4:7], s47 offen nt
	s_mov_b32 s40, 0x10e480
	s_mov_b32 s41, 0x130110
	s_mov_b32 s42, 0x151da0
	s_mov_b32 s43, 0x173a30
	s_mov_b32 s44, 0x1956c0
	s_mov_b32 s45, 0x1b7350
	s_mov_b32 s46, 0x1d8fe0
	s_mov_b32 s47, 0x1fac70
	buffer_load_dwordx2 v[60:61], v3, s[4:7], s40 offen nt
	buffer_load_dwordx2 v[62:63], v3, s[4:7], s41 offen nt
	buffer_load_dwordx2 v[64:65], v3, s[4:7], s42 offen nt
	buffer_load_dwordx2 v[66:67], v3, s[4:7], s43 offen nt
	buffer_load_dwordx2 v[68:69], v3, s[4:7], s44 offen nt
	buffer_load_dwordx2 v[70:71], v3, s[4:7], s45 offen nt
	buffer_load_dwordx2 v[72:73], v3, s[4:7], s46 offen nt
	buffer_load_dwordx2 v[74:75], v3, s[4:7], s47 offen nt
	s_mov_b32 s40, 0x21c900
	s_mov_b32 s41, 0x23e590
	s_mov_b32 s42, 0x260220
	s_mov_b32 s43, 0x281eb0
	s_mov_b32 s44, 0x2a3b40
	s_mov_b32 s45, 0x2c57d0
	s_mov_b32 s46, 0x2e7460
	s_mov_b32 s47, 0x3090f0
	buffer_load_dwordx2 v[76:77], v3, s[4:7], s40 offen nt
	buffer_load_dwordx2 v[78:79], v3, s[4:7], s41 offen nt
	buffer_load_dwordx2 v[80:81], v3, s[4:7], s42 offen nt
	buffer_load_dwordx2 v[82:83], v3, s[4:7], s43 offen nt
	buffer_load_dwordx2 v[84:85], v3, s[4:7], s44 offen nt
	buffer_load_dwordx2 v[86:87], v3, s[4:7], s45 offen nt
	buffer_load_dwordx2 v[88:89], v3, s[4:7], s46 offen nt
	buffer_load_dwordx2 v[90:91], v3, s[4:7], s47 offen nt
	s_mov_b32 s40, 0x32ad80
	s_mov_b32 s41, 0x34ca10
	s_mov_b32 s42, 0x36e6a0
	s_mov_b32 s43, 0x390330
	s_mov_b32 s44, 0x3b1fc0
	s_mov_b32 s45, 0x3d3c50
	s_mov_b32 s46, 0x3f58e0
	s_mov_b32 s47, 0x417570
	buffer_load_dwordx2 v[92:93], v3, s[4:7], s40 offen nt
	buffer_load_dwordx2 v[94:95], v3, s[4:7], s41 offen nt
	buffer_load_dwordx2 v[96:97], v3, s[4:7], s42 offen nt
	buffer_load_dwordx2 v[98:99], v3, s[4:7], s43 offen nt
	buffer_load_dwordx2 v[100:101], v3, s[4:7], s44 offen nt
	buffer_load_dwordx2 v[102:103], v3, s[4:7], s45 offen nt
	buffer_load_dwordx2 v[104:105], v3, s[4:7], s46 offen nt
	buffer_load_dwordx2 v[106:107], v3, s[4:7], s47 offen nt
	s_mov_b32 s40, 0x0
	s_mov_b32 s41, 0x400
	s_mov_b32 s42, 0x800
	s_mov_b32 s43, 0xc00
	buffer_load_dwordx4 v[108:111], v4, s[8:11], s40 offen
	buffer_load_dwordx4 v[112:115], v4, s[8:11], s41 offen
	buffer_load_dwordx4 v[116:119], v4, s[8:11], s42 offen
	buffer_load_dwordx4 v[120:123], v4, s[8:11], s43 offen
	s_mov_b32 s40, 0x1000
	s_mov_b32 s41, 0x1400
	s_mov_b32 s42, 0x1800
	s_mov_b32 s43, 0x1c00
	buffer_load_dwordx4 v[124:127], v4, s[8:11], s40 offen
	buffer_load_dwordx4 v[128:131], v4, s[8:11], s41 offen
	buffer_load_dwordx4 v[132:135], v4, s[8:11], s42 offen
	buffer_load_dwordx4 v[136:139], v4, s[8:11], s43 offen
	s_mov_b32 s40, 0x10000
	s_mov_b32 s41, 0x10400
	s_mov_b32 s42, 0x10800
	s_mov_b32 s43, 0x10c00
	buffer_load_dwordx4 v[148:151], v4, s[8:11], s40 offen
	buffer_load_dwordx4 v[152:155], v4, s[8:11], s41 offen
	buffer_load_dwordx4 v[156:159], v4, s[8:11], s42 offen
	buffer_load_dwordx4 v[160:163], v4, s[8:11], s43 offen
	s_mov_b32 s40, 0x11000
	s_mov_b32 s41, 0x11400
	s_mov_b32 s42, 0x11800
	s_mov_b32 s43, 0x11c00
	buffer_load_dwordx4 v[164:167], v4, s[8:11], s40 offen
	buffer_load_dwordx4 v[168:171], v4, s[8:11], s41 offen
	buffer_load_dwordx4 v[172:175], v4, s[8:11], s42 offen
	buffer_load_dwordx4 v[176:179], v4, s[8:11], s43 offen
	s_waitcnt vmcnt(40)
	v_cvt_pkrtz_f16_f32 v12, v44, v46
	v_cvt_pkrtz_f16_f32 v13, v48, v50
	v_cvt_pkrtz_f16_f32 v14, v52, v54
	v_cvt_pkrtz_f16_f32 v15, v56, v58
	v_cvt_pkrtz_f16_f32 v16, v45, v47
	v_cvt_pkrtz_f16_f32 v17, v49, v51
	v_cvt_pkrtz_f16_f32 v18, v53, v55
	v_cvt_pkrtz_f16_f32 v19, v57, v59
	ds_write_b128 v5, v[12:15] offset:0
	ds_write_b128 v5, v[16:19] offset:2048
	s_waitcnt vmcnt(32)
	v_cvt_pkrtz_f16_f32 v12, v60, v62
	v_cvt_pkrtz_f16_f32 v13, v64, v66
	v_cvt_pkrtz_f16_f32 v14, v68, v70
	v_cvt_pkrtz_f16_f32 v15, v72, v74
	v_cvt_pkrtz_f16_f32 v16, v61, v63
	v_cvt_pkrtz_f16_f32 v17, v65, v67
	v_cvt_pkrtz_f16_f32 v18, v69, v71
	v_cvt_pkrtz_f16_f32 v19, v73, v75
	s_mov_b32 s40, 0x3c10
	s_mov_b32 s41, 0x258a0
	s_mov_b32 s42, 0x47530
	s_mov_b32 s43, 0x691c0
	s_mov_b32 s44, 0x8ae50
	s_mov_b32 s45, 0xacae0
	s_mov_b32 s46, 0xce770
	s_mov_b32 s47, 0xf0400
	buffer_load_dwordx2 v[44:45], v3, s[4:7], s40 offen nt
	buffer_load_dwordx2 v[46:47], v3, s[4:7], s41 offen nt
	buffer_load_dwordx2 v[48:49], v3, s[4:7], s42 offen nt
	buffer_load_dwordx2 v[50:51], v3, s[4:7], s43 offen nt
	buffer_load_dwordx2 v[52:53], v3, s[4:7], s44 offen nt
	buffer_load_dwordx2 v[54:55], v3, s[4:7], s45 offen nt
	buffer_load_dwordx2 v[56:57], v3, s[4:7], s46 offen nt
	buffer_load_dwordx2 v[58:59], v3, s[4:7], s47 offen nt
	ds_write_b128 v5, v[12:15] offset:256
	ds_write_b128 v5, v[16:19] offset:2304
	s_waitcnt vmcnt(32)
	v_cvt_pkrtz_f16_f32 v12, v76, v78
	v_cvt_pkrtz_f16_f32 v13, v80, v82
	v_cvt_pkrtz_f16_f32 v14, v84, v86
	v_cvt_pkrtz_f16_f32 v15, v88, v90
	v_cvt_pkrtz_f16_f32 v16, v77, v79
	v_cvt_pkrtz_f16_f32 v17, v81, v83
	v_cvt_pkrtz_f16_f32 v18, v85, v87
	v_cvt_pkrtz_f16_f32 v19, v89, v91
	s_mov_b32 s40, 0x112090
	s_mov_b32 s41, 0x133d20
	s_mov_b32 s42, 0x1559b0
	s_mov_b32 s43, 0x177640
	s_mov_b32 s44, 0x1992d0
	s_mov_b32 s45, 0x1baf60
	s_mov_b32 s46, 0x1dcbf0
	s_mov_b32 s47, 0x1fe880
	buffer_load_dwordx2 v[60:61], v3, s[4:7], s40 offen nt
	buffer_load_dwordx2 v[62:63], v3, s[4:7], s41 offen nt
	buffer_load_dwordx2 v[64:65], v3, s[4:7], s42 offen nt
	buffer_load_dwordx2 v[66:67], v3, s[4:7], s43 offen nt
	buffer_load_dwordx2 v[68:69], v3, s[4:7], s44 offen nt
	buffer_load_dwordx2 v[70:71], v3, s[4:7], s45 offen nt
	buffer_load_dwordx2 v[72:73], v3, s[4:7], s46 offen nt
	buffer_load_dwordx2 v[74:75], v3, s[4:7], s47 offen nt
	ds_write_b128 v5, v[12:15] offset:512
	ds_write_b128 v5, v[16:19] offset:2560
	s_waitcnt vmcnt(32)
	v_cvt_pkrtz_f16_f32 v12, v92, v94
	v_cvt_pkrtz_f16_f32 v13, v96, v98
	v_cvt_pkrtz_f16_f32 v14, v100, v102
	v_cvt_pkrtz_f16_f32 v15, v104, v106
	v_cvt_pkrtz_f16_f32 v16, v93, v95
	v_cvt_pkrtz_f16_f32 v17, v97, v99
	v_cvt_pkrtz_f16_f32 v18, v101, v103
	v_cvt_pkrtz_f16_f32 v19, v105, v107
	s_mov_b32 s40, 0x220510
	s_mov_b32 s41, 0x2421a0
	s_mov_b32 s42, 0x263e30
	s_mov_b32 s43, 0x285ac0
	s_mov_b32 s44, 0x2a7750
	s_mov_b32 s45, 0x2c93e0
	s_mov_b32 s46, 0x2eb070
	s_mov_b32 s47, 0x30cd00
	buffer_load_dwordx2 v[76:77], v3, s[4:7], s40 offen nt
	buffer_load_dwordx2 v[78:79], v3, s[4:7], s41 offen nt
	buffer_load_dwordx2 v[80:81], v3, s[4:7], s42 offen nt
	buffer_load_dwordx2 v[82:83], v3, s[4:7], s43 offen nt
	buffer_load_dwordx2 v[84:85], v3, s[4:7], s44 offen nt
	buffer_load_dwordx2 v[86:87], v3, s[4:7], s45 offen nt
	buffer_load_dwordx2 v[88:89], v3, s[4:7], s46 offen nt
	buffer_load_dwordx2 v[90:91], v3, s[4:7], s47 offen nt
	ds_write_b128 v5, v[12:15] offset:768
	ds_write_b128 v5, v[16:19] offset:2816
	s_waitcnt lgkmcnt(0)
	s_barrier
	s_waitcnt vmcnt(24)
	ds_write_b128 v254, v[108:111] offset:0
	ds_write_b128 v254, v[112:115] offset:1024
	ds_write_b128 v254, v[148:151] offset:16384
	ds_write_b128 v254, v[152:155] offset:17408
	s_waitcnt lgkmcnt(0)
	s_barrier
	ds_read_b128 v[140:143], v255 offset:0
	ds_read_b128 v[144:147], v255 offset:1024
	ds_read_b128 v[180:183], v255 offset:16384
	ds_read_b128 v[184:187], v255 offset:17408
	ds_read_b128 v[12:15], v6 offset:0
	ds_read_b128 v[16:19], v6 offset:2048
	ds_read_b128 v[20:23], v7 offset:0
	ds_read_b128 v[24:27], v7 offset:2048
	ds_read_b128 v[28:31], v8 offset:0
	ds_read_b128 v[32:35], v8 offset:2048
	ds_read_b128 v[36:39], v9 offset:0
	ds_read_b128 v[40:43], v9 offset:2048
	s_waitcnt lgkmcnt(7)
	v_mfma_f32_16x16x32_f16 v[188:191], v[108:111], v[12:15], 0
	v_mfma_f32_16x16x32_f16 v[220:223], v[148:151], v[12:15], 0
	s_waitcnt lgkmcnt(6)
	v_mfma_f32_16x16x32_f16 v[192:195], v[112:115], v[16:19], 0
	v_mfma_f32_16x16x32_f16 v[224:227], v[152:155], v[16:19], 0
	s_waitcnt lgkmcnt(5)
	v_mfma_f32_16x16x32_f16 v[196:199], v[116:119], v[20:23], 0
	v_mfma_f32_16x16x32_f16 v[228:231], v[156:159], v[20:23], 0
	s_waitcnt lgkmcnt(4)
	v_mfma_f32_16x16x32_f16 v[200:203], v[120:123], v[24:27], 0
	v_mfma_f32_16x16x32_f16 v[232:235], v[160:163], v[24:27], 0
	s_waitcnt lgkmcnt(3)
	v_mfma_f32_16x16x32_f16 v[204:207], v[124:127], v[28:31], 0
	v_mfma_f32_16x16x32_f16 v[236:239], v[164:167], v[28:31], 0
	s_waitcnt lgkmcnt(2)
	v_mfma_f32_16x16x32_f16 v[208:211], v[128:131], v[32:35], 0
	v_mfma_f32_16x16x32_f16 v[240:243], v[168:171], v[32:35], 0
	s_waitcnt lgkmcnt(1)
	v_mfma_f32_16x16x32_f16 v[212:215], v[132:135], v[36:39], 0
	v_mfma_f32_16x16x32_f16 v[244:247], v[172:175], v[36:39], 0
	s_waitcnt lgkmcnt(0)
	v_mfma_f32_16x16x32_f16 v[216:219], v[136:139], v[40:43], 0
	v_mfma_f32_16x16x32_f16 v[248:251], v[176:179], v[40:43], 0
	s_mov_b32 s40, 0x32e990
	s_mov_b32 s41, 0x350620
	s_mov_b32 s42, 0x3722b0
	s_mov_b32 s43, 0x393f40
	s_mov_b32 s44, 0x3b5bd0
	s_mov_b32 s45, 0x3d7860
	s_mov_b32 s46, 0x3f94f0
	s_mov_b32 s47, 0x41b180
	buffer_load_dwordx2 v[92:93], v3, s[4:7], s40 offen nt
	buffer_load_dwordx2 v[94:95], v3, s[4:7], s41 offen nt
	buffer_load_dwordx2 v[96:97], v3, s[4:7], s42 offen nt
	buffer_load_dwordx2 v[98:99], v3, s[4:7], s43 offen nt
	buffer_load_dwordx2 v[100:101], v3, s[4:7], s44 offen nt
	buffer_load_dwordx2 v[102:103], v3, s[4:7], s45 offen nt
	buffer_load_dwordx2 v[104:105], v3, s[4:7], s46 offen nt
	buffer_load_dwordx2 v[106:107], v3, s[4:7], s47 offen nt
	s_waitcnt vmcnt(24)
	v_cvt_pkrtz_f16_f32 v12, v44, v46
	v_cvt_pkrtz_f16_f32 v13, v48, v50
	v_cvt_pkrtz_f16_f32 v14, v52, v54
	v_cvt_pkrtz_f16_f32 v15, v56, v58
	v_cvt_pkrtz_f16_f32 v16, v45, v47
	v_cvt_pkrtz_f16_f32 v17, v49, v51
	v_cvt_pkrtz_f16_f32 v18, v53, v55
	v_cvt_pkrtz_f16_f32 v19, v57, v59
	ds_write_b128 v5, v[12:15] offset:1024
	ds_write_b128 v5, v[16:19] offset:3072
	s_waitcnt vmcnt(16)
	v_cvt_pkrtz_f16_f32 v12, v60, v62
	v_cvt_pkrtz_f16_f32 v13, v64, v66
	v_cvt_pkrtz_f16_f32 v14, v68, v70
	v_cvt_pkrtz_f16_f32 v15, v72, v74
	v_cvt_pkrtz_f16_f32 v16, v61, v63
	v_cvt_pkrtz_f16_f32 v17, v65, v67
	v_cvt_pkrtz_f16_f32 v18, v69, v71
	v_cvt_pkrtz_f16_f32 v19, v73, v75
	s_mov_b32 s40, 0x7820
	s_mov_b32 s41, 0x294b0
	s_mov_b32 s42, 0x4b140
	s_mov_b32 s43, 0x6cdd0
	s_mov_b32 s44, 0x8ea60
	s_mov_b32 s45, 0xb06f0
	s_mov_b32 s46, 0xd2380
	s_mov_b32 s47, 0xf4010
	buffer_load_dwordx2 v[44:45], v3, s[4:7], s40 offen nt
	buffer_load_dwordx2 v[46:47], v3, s[4:7], s41 offen nt
	buffer_load_dwordx2 v[48:49], v3, s[4:7], s42 offen nt
	buffer_load_dwordx2 v[50:51], v3, s[4:7], s43 offen nt
	buffer_load_dwordx2 v[52:53], v3, s[4:7], s44 offen nt
	buffer_load_dwordx2 v[54:55], v3, s[4:7], s45 offen nt
	buffer_load_dwordx2 v[56:57], v3, s[4:7], s46 offen nt
	buffer_load_dwordx2 v[58:59], v3, s[4:7], s47 offen nt
	ds_write_b128 v5, v[12:15] offset:1280
	ds_write_b128 v5, v[16:19] offset:3328
	s_waitcnt vmcnt(16)
	v_cvt_pkrtz_f16_f32 v12, v76, v78
	v_cvt_pkrtz_f16_f32 v13, v80, v82
	v_cvt_pkrtz_f16_f32 v14, v84, v86
	v_cvt_pkrtz_f16_f32 v15, v88, v90
	v_cvt_pkrtz_f16_f32 v16, v77, v79
	v_cvt_pkrtz_f16_f32 v17, v81, v83
	v_cvt_pkrtz_f16_f32 v18, v85, v87
	v_cvt_pkrtz_f16_f32 v19, v89, v91
	s_mov_b32 s40, 0x115ca0
	s_mov_b32 s41, 0x137930
	s_mov_b32 s42, 0x1595c0
	s_mov_b32 s43, 0x17b250
	s_mov_b32 s44, 0x19cee0
	s_mov_b32 s45, 0x1beb70
	s_mov_b32 s46, 0x1e0800
	s_mov_b32 s47, 0x202490
	buffer_load_dwordx2 v[60:61], v3, s[4:7], s40 offen nt
	buffer_load_dwordx2 v[62:63], v3, s[4:7], s41 offen nt
	buffer_load_dwordx2 v[64:65], v3, s[4:7], s42 offen nt
	buffer_load_dwordx2 v[66:67], v3, s[4:7], s43 offen nt
	buffer_load_dwordx2 v[68:69], v3, s[4:7], s44 offen nt
	buffer_load_dwordx2 v[70:71], v3, s[4:7], s45 offen nt
	buffer_load_dwordx2 v[72:73], v3, s[4:7], s46 offen nt
	buffer_load_dwordx2 v[74:75], v3, s[4:7], s47 offen nt
	ds_write_b128 v5, v[12:15] offset:1536
	ds_write_b128 v5, v[16:19] offset:3584
	s_waitcnt vmcnt(16)
	v_cvt_pkrtz_f16_f32 v12, v92, v94
	v_cvt_pkrtz_f16_f32 v13, v96, v98
	v_cvt_pkrtz_f16_f32 v14, v100, v102
	v_cvt_pkrtz_f16_f32 v15, v104, v106
	v_cvt_pkrtz_f16_f32 v16, v93, v95
	v_cvt_pkrtz_f16_f32 v17, v97, v99
	v_cvt_pkrtz_f16_f32 v18, v101, v103
	v_cvt_pkrtz_f16_f32 v19, v105, v107
	s_mov_b32 s40, 0x224120
	s_mov_b32 s41, 0x245db0
	s_mov_b32 s42, 0x267a40
	s_mov_b32 s43, 0x2896d0
	s_mov_b32 s44, 0x2ab360
	s_mov_b32 s45, 0x2ccff0
	s_mov_b32 s46, 0x2eec80
	s_mov_b32 s47, 0x310910
	buffer_load_dwordx2 v[76:77], v3, s[4:7], s40 offen nt
	buffer_load_dwordx2 v[78:79], v3, s[4:7], s41 offen nt
	buffer_load_dwordx2 v[80:81], v3, s[4:7], s42 offen nt
	buffer_load_dwordx2 v[82:83], v3, s[4:7], s43 offen nt
	buffer_load_dwordx2 v[84:85], v3, s[4:7], s44 offen nt
	buffer_load_dwordx2 v[86:87], v3, s[4:7], s45 offen nt
	buffer_load_dwordx2 v[88:89], v3, s[4:7], s46 offen nt
	buffer_load_dwordx2 v[90:91], v3, s[4:7], s47 offen nt
	ds_write_b128 v5, v[12:15] offset:1792
	ds_write_b128 v5, v[16:19] offset:3840
	s_waitcnt lgkmcnt(0)
	s_barrier
	ds_read_b128 v[12:15], v6 offset:1024
	ds_read_b128 v[16:19], v6 offset:3072
	ds_read_b128 v[20:23], v7 offset:1024
	ds_read_b128 v[24:27], v7 offset:3072
	ds_read_b128 v[28:31], v8 offset:1024
	ds_read_b128 v[32:35], v8 offset:3072
	ds_read_b128 v[36:39], v9 offset:1024
	ds_read_b128 v[40:43], v9 offset:3072
	s_waitcnt lgkmcnt(7)
	v_mfma_f32_16x16x32_f16 v[188:191], v[112:115], v[12:15], v[188:191]
	v_mfma_f32_16x16x32_f16 v[220:223], v[152:155], v[12:15], v[220:223]
	s_waitcnt lgkmcnt(6)
	v_mfma_f32_16x16x32_f16 v[192:195], v[116:119], v[16:19], v[192:195]
	v_mfma_f32_16x16x32_f16 v[224:227], v[156:159], v[16:19], v[224:227]
	s_waitcnt lgkmcnt(5)
	v_mfma_f32_16x16x32_f16 v[196:199], v[120:123], v[20:23], v[196:199]
	v_mfma_f32_16x16x32_f16 v[228:231], v[160:163], v[20:23], v[228:231]
	s_waitcnt lgkmcnt(4)
	v_mfma_f32_16x16x32_f16 v[200:203], v[124:127], v[24:27], v[200:203]
	v_mfma_f32_16x16x32_f16 v[232:235], v[164:167], v[24:27], v[232:235]
	s_waitcnt lgkmcnt(3)
	v_mfma_f32_16x16x32_f16 v[204:207], v[128:131], v[28:31], v[204:207]
	v_mfma_f32_16x16x32_f16 v[236:239], v[168:171], v[28:31], v[236:239]
	s_waitcnt lgkmcnt(2)
	v_mfma_f32_16x16x32_f16 v[208:211], v[132:135], v[32:35], v[208:211]
	v_mfma_f32_16x16x32_f16 v[240:243], v[172:175], v[32:35], v[240:243]
	s_waitcnt lgkmcnt(1)
	v_mfma_f32_16x16x32_f16 v[212:215], v[136:139], v[36:39], v[212:215]
	v_mfma_f32_16x16x32_f16 v[244:247], v[176:179], v[36:39], v[244:247]
	s_waitcnt lgkmcnt(0)
	v_mfma_f32_16x16x32_f16 v[216:219], v[140:143], v[40:43], v[216:219]
	v_mfma_f32_16x16x32_f16 v[248:251], v[180:183], v[40:43], v[248:251]
	s_mov_b32 s40, 0x3325a0
	s_mov_b32 s41, 0x354230
	s_mov_b32 s42, 0x375ec0
	s_mov_b32 s43, 0x397b50
	s_mov_b32 s44, 0x3b97e0
	s_mov_b32 s45, 0x3db470
	s_mov_b32 s46, 0x3fd100
	s_mov_b32 s47, 0x41ed90
	buffer_load_dwordx2 v[92:93], v3, s[4:7], s40 offen nt
	buffer_load_dwordx2 v[94:95], v3, s[4:7], s41 offen nt
	buffer_load_dwordx2 v[96:97], v3, s[4:7], s42 offen nt
	buffer_load_dwordx2 v[98:99], v3, s[4:7], s43 offen nt
	buffer_load_dwordx2 v[100:101], v3, s[4:7], s44 offen nt
	buffer_load_dwordx2 v[102:103], v3, s[4:7], s45 offen nt
	buffer_load_dwordx2 v[104:105], v3, s[4:7], s46 offen nt
	buffer_load_dwordx2 v[106:107], v3, s[4:7], s47 offen nt
	s_waitcnt vmcnt(24)
	v_cvt_pkrtz_f16_f32 v12, v44, v46
	v_cvt_pkrtz_f16_f32 v13, v48, v50
	v_cvt_pkrtz_f16_f32 v14, v52, v54
	v_cvt_pkrtz_f16_f32 v15, v56, v58
	v_cvt_pkrtz_f16_f32 v16, v45, v47
	v_cvt_pkrtz_f16_f32 v17, v49, v51
	v_cvt_pkrtz_f16_f32 v18, v53, v55
	v_cvt_pkrtz_f16_f32 v19, v57, v59
	ds_write_b128 v5, v[12:15] offset:0
	ds_write_b128 v5, v[16:19] offset:2048
	s_waitcnt vmcnt(16)
	v_cvt_pkrtz_f16_f32 v12, v60, v62
	v_cvt_pkrtz_f16_f32 v13, v64, v66
	v_cvt_pkrtz_f16_f32 v14, v68, v70
	v_cvt_pkrtz_f16_f32 v15, v72, v74
	v_cvt_pkrtz_f16_f32 v16, v61, v63
	v_cvt_pkrtz_f16_f32 v17, v65, v67
	v_cvt_pkrtz_f16_f32 v18, v69, v71
	v_cvt_pkrtz_f16_f32 v19, v73, v75
	s_mov_b32 s40, 0xb430
	s_mov_b32 s41, 0x2d0c0
	s_mov_b32 s42, 0x4ed50
	s_mov_b32 s43, 0x709e0
	s_mov_b32 s44, 0x92670
	s_mov_b32 s45, 0xb4300
	s_mov_b32 s46, 0xd5f90
	s_mov_b32 s47, 0xf7c20
	buffer_load_dwordx2 v[44:45], v3, s[4:7], s40 offen nt
	buffer_load_dwordx2 v[46:47], v3, s[4:7], s41 offen nt
	buffer_load_dwordx2 v[48:49], v3, s[4:7], s42 offen nt
	buffer_load_dwordx2 v[50:51], v3, s[4:7], s43 offen nt
	buffer_load_dwordx2 v[52:53], v3, s[4:7], s44 offen nt
	buffer_load_dwordx2 v[54:55], v3, s[4:7], s45 offen nt
	buffer_load_dwordx2 v[56:57], v3, s[4:7], s46 offen nt
	buffer_load_dwordx2 v[58:59], v3, s[4:7], s47 offen nt
	ds_write_b128 v5, v[12:15] offset:256
	ds_write_b128 v5, v[16:19] offset:2304
	s_waitcnt vmcnt(16)
	v_cvt_pkrtz_f16_f32 v12, v76, v78
	v_cvt_pkrtz_f16_f32 v13, v80, v82
	v_cvt_pkrtz_f16_f32 v14, v84, v86
	v_cvt_pkrtz_f16_f32 v15, v88, v90
	v_cvt_pkrtz_f16_f32 v16, v77, v79
	v_cvt_pkrtz_f16_f32 v17, v81, v83
	v_cvt_pkrtz_f16_f32 v18, v85, v87
	v_cvt_pkrtz_f16_f32 v19, v89, v91
	s_mov_b32 s40, 0x1198b0
	s_mov_b32 s41, 0x13b540
	s_mov_b32 s42, 0x15d1d0
	s_mov_b32 s43, 0x17ee60
	s_mov_b32 s44, 0x1a0af0
	s_mov_b32 s45, 0x1c2780
	s_mov_b32 s46, 0x1e4410
	s_mov_b32 s47, 0x2060a0
	buffer_load_dwordx2 v[60:61], v3, s[4:7], s40 offen nt
	buffer_load_dwordx2 v[62:63], v3, s[4:7], s41 offen nt
	buffer_load_dwordx2 v[64:65], v3, s[4:7], s42 offen nt
	buffer_load_dwordx2 v[66:67], v3, s[4:7], s43 offen nt
	buffer_load_dwordx2 v[68:69], v3, s[4:7], s44 offen nt
	buffer_load_dwordx2 v[70:71], v3, s[4:7], s45 offen nt
	buffer_load_dwordx2 v[72:73], v3, s[4:7], s46 offen nt
	buffer_load_dwordx2 v[74:75], v3, s[4:7], s47 offen nt
	ds_write_b128 v5, v[12:15] offset:512
	ds_write_b128 v5, v[16:19] offset:2560
	s_waitcnt vmcnt(16)
	v_cvt_pkrtz_f16_f32 v12, v92, v94
	v_cvt_pkrtz_f16_f32 v13, v96, v98
	v_cvt_pkrtz_f16_f32 v14, v100, v102
	v_cvt_pkrtz_f16_f32 v15, v104, v106
	v_cvt_pkrtz_f16_f32 v16, v93, v95
	v_cvt_pkrtz_f16_f32 v17, v97, v99
	v_cvt_pkrtz_f16_f32 v18, v101, v103
	v_cvt_pkrtz_f16_f32 v19, v105, v107
	s_mov_b32 s40, 0x227d30
	s_mov_b32 s41, 0x2499c0
	s_mov_b32 s42, 0x26b650
	s_mov_b32 s43, 0x28d2e0
	s_mov_b32 s44, 0x2aef70
	s_mov_b32 s45, 0x2d0c00
	s_mov_b32 s46, 0x2f2890
	s_mov_b32 s47, 0x314520
	buffer_load_dwordx2 v[76:77], v3, s[4:7], s40 offen nt
	buffer_load_dwordx2 v[78:79], v3, s[4:7], s41 offen nt
	buffer_load_dwordx2 v[80:81], v3, s[4:7], s42 offen nt
	buffer_load_dwordx2 v[82:83], v3, s[4:7], s43 offen nt
	buffer_load_dwordx2 v[84:85], v3, s[4:7], s44 offen nt
	buffer_load_dwordx2 v[86:87], v3, s[4:7], s45 offen nt
	buffer_load_dwordx2 v[88:89], v3, s[4:7], s46 offen nt
	buffer_load_dwordx2 v[90:91], v3, s[4:7], s47 offen nt
	ds_write_b128 v5, v[12:15] offset:768
	ds_write_b128 v5, v[16:19] offset:2816
	s_waitcnt lgkmcnt(0)
	s_barrier
	ds_read_b128 v[12:15], v6 offset:0
	ds_read_b128 v[16:19], v6 offset:2048
	ds_read_b128 v[20:23], v7 offset:0
	ds_read_b128 v[24:27], v7 offset:2048
	ds_read_b128 v[28:31], v8 offset:0
	ds_read_b128 v[32:35], v8 offset:2048
	ds_read_b128 v[36:39], v9 offset:0
	ds_read_b128 v[40:43], v9 offset:2048
	s_waitcnt lgkmcnt(7)
	v_mfma_f32_16x16x32_f16 v[188:191], v[116:119], v[12:15], v[188:191]
	v_mfma_f32_16x16x32_f16 v[220:223], v[156:159], v[12:15], v[220:223]
	s_waitcnt lgkmcnt(6)
	v_mfma_f32_16x16x32_f16 v[192:195], v[120:123], v[16:19], v[192:195]
	v_mfma_f32_16x16x32_f16 v[224:227], v[160:163], v[16:19], v[224:227]
	s_waitcnt lgkmcnt(5)
	v_mfma_f32_16x16x32_f16 v[196:199], v[124:127], v[20:23], v[196:199]
	v_mfma_f32_16x16x32_f16 v[228:231], v[164:167], v[20:23], v[228:231]
	s_waitcnt lgkmcnt(4)
	v_mfma_f32_16x16x32_f16 v[200:203], v[128:131], v[24:27], v[200:203]
	v_mfma_f32_16x16x32_f16 v[232:235], v[168:171], v[24:27], v[232:235]
	s_waitcnt lgkmcnt(3)
	v_mfma_f32_16x16x32_f16 v[204:207], v[132:135], v[28:31], v[204:207]
	v_mfma_f32_16x16x32_f16 v[236:239], v[172:175], v[28:31], v[236:239]
	s_waitcnt lgkmcnt(2)
	v_mfma_f32_16x16x32_f16 v[208:211], v[136:139], v[32:35], v[208:211]
	v_mfma_f32_16x16x32_f16 v[240:243], v[176:179], v[32:35], v[240:243]
	s_waitcnt lgkmcnt(1)
	v_mfma_f32_16x16x32_f16 v[212:215], v[140:143], v[36:39], v[212:215]
	v_mfma_f32_16x16x32_f16 v[244:247], v[180:183], v[36:39], v[244:247]
	s_waitcnt lgkmcnt(0)
	v_mfma_f32_16x16x32_f16 v[216:219], v[144:147], v[40:43], v[216:219]
	v_mfma_f32_16x16x32_f16 v[248:251], v[184:187], v[40:43], v[248:251]
	s_mov_b32 s40, 0x20000
	s_mov_b32 s41, 0x20400
	s_mov_b32 s42, 0x20800
	s_mov_b32 s43, 0x20c00
	buffer_load_dwordx4 v[108:111], v4, s[8:11], s40 offen
	buffer_load_dwordx4 v[112:115], v4, s[8:11], s41 offen
	buffer_load_dwordx4 v[116:119], v4, s[8:11], s42 offen
	buffer_load_dwordx4 v[120:123], v4, s[8:11], s43 offen
	s_mov_b32 s40, 0x21000
	s_mov_b32 s41, 0x21400
	s_mov_b32 s42, 0x21800
	s_mov_b32 s43, 0x21c00
	buffer_load_dwordx4 v[124:127], v4, s[8:11], s40 offen
	buffer_load_dwordx4 v[128:131], v4, s[8:11], s41 offen
	buffer_load_dwordx4 v[132:135], v4, s[8:11], s42 offen
	buffer_load_dwordx4 v[136:139], v4, s[8:11], s43 offen
	s_mov_b32 s40, 0x3361b0
	s_mov_b32 s41, 0x357e40
	s_mov_b32 s42, 0x379ad0
	s_mov_b32 s43, 0x39b760
	s_mov_b32 s44, 0x3bd3f0
	s_mov_b32 s45, 0x3df080
	s_mov_b32 s46, 0x400d10
	s_mov_b32 s47, 0x4229a0
	buffer_load_dwordx2 v[92:93], v3, s[4:7], s40 offen nt
	buffer_load_dwordx2 v[94:95], v3, s[4:7], s41 offen nt
	buffer_load_dwordx2 v[96:97], v3, s[4:7], s42 offen nt
	buffer_load_dwordx2 v[98:99], v3, s[4:7], s43 offen nt
	buffer_load_dwordx2 v[100:101], v3, s[4:7], s44 offen nt
	buffer_load_dwordx2 v[102:103], v3, s[4:7], s45 offen nt
	buffer_load_dwordx2 v[104:105], v3, s[4:7], s46 offen nt
	buffer_load_dwordx2 v[106:107], v3, s[4:7], s47 offen nt
	s_waitcnt vmcnt(32)
	v_cvt_pkrtz_f16_f32 v12, v44, v46
	v_cvt_pkrtz_f16_f32 v13, v48, v50
	v_cvt_pkrtz_f16_f32 v14, v52, v54
	v_cvt_pkrtz_f16_f32 v15, v56, v58
	v_cvt_pkrtz_f16_f32 v16, v45, v47
	v_cvt_pkrtz_f16_f32 v17, v49, v51
	v_cvt_pkrtz_f16_f32 v18, v53, v55
	v_cvt_pkrtz_f16_f32 v19, v57, v59
	ds_write_b128 v5, v[12:15] offset:1024
	ds_write_b128 v5, v[16:19] offset:3072
	s_waitcnt vmcnt(24)
	v_cvt_pkrtz_f16_f32 v12, v60, v62
	v_cvt_pkrtz_f16_f32 v13, v64, v66
	v_cvt_pkrtz_f16_f32 v14, v68, v70
	v_cvt_pkrtz_f16_f32 v15, v72, v74
	v_cvt_pkrtz_f16_f32 v16, v61, v63
	v_cvt_pkrtz_f16_f32 v17, v65, v67
	v_cvt_pkrtz_f16_f32 v18, v69, v71
	v_cvt_pkrtz_f16_f32 v19, v73, v75
	s_mov_b32 s40, 0xf040
	s_mov_b32 s41, 0x30cd0
	s_mov_b32 s42, 0x52960
	s_mov_b32 s43, 0x745f0
	s_mov_b32 s44, 0x96280
	s_mov_b32 s45, 0xb7f10
	s_mov_b32 s46, 0xd9ba0
	s_mov_b32 s47, 0xfb830
	buffer_load_dwordx2 v[44:45], v3, s[4:7], s40 offen nt
	buffer_load_dwordx2 v[46:47], v3, s[4:7], s41 offen nt
	buffer_load_dwordx2 v[48:49], v3, s[4:7], s42 offen nt
	buffer_load_dwordx2 v[50:51], v3, s[4:7], s43 offen nt
	buffer_load_dwordx2 v[52:53], v3, s[4:7], s44 offen nt
	buffer_load_dwordx2 v[54:55], v3, s[4:7], s45 offen nt
	buffer_load_dwordx2 v[56:57], v3, s[4:7], s46 offen nt
	buffer_load_dwordx2 v[58:59], v3, s[4:7], s47 offen nt
	ds_write_b128 v5, v[12:15] offset:1280
	ds_write_b128 v5, v[16:19] offset:3328
	s_waitcnt vmcnt(24)
	v_cvt_pkrtz_f16_f32 v12, v76, v78
	v_cvt_pkrtz_f16_f32 v13, v80, v82
	v_cvt_pkrtz_f16_f32 v14, v84, v86
	v_cvt_pkrtz_f16_f32 v15, v88, v90
	v_cvt_pkrtz_f16_f32 v16, v77, v79
	v_cvt_pkrtz_f16_f32 v17, v81, v83
	v_cvt_pkrtz_f16_f32 v18, v85, v87
	v_cvt_pkrtz_f16_f32 v19, v89, v91
	s_mov_b32 s40, 0x11d4c0
	s_mov_b32 s41, 0x13f150
	s_mov_b32 s42, 0x160de0
	s_mov_b32 s43, 0x182a70
	s_mov_b32 s44, 0x1a4700
	s_mov_b32 s45, 0x1c6390
	s_mov_b32 s46, 0x1e8020
	s_mov_b32 s47, 0x209cb0
	buffer_load_dwordx2 v[60:61], v3, s[4:7], s40 offen nt
	buffer_load_dwordx2 v[62:63], v3, s[4:7], s41 offen nt
	buffer_load_dwordx2 v[64:65], v3, s[4:7], s42 offen nt
	buffer_load_dwordx2 v[66:67], v3, s[4:7], s43 offen nt
	buffer_load_dwordx2 v[68:69], v3, s[4:7], s44 offen nt
	buffer_load_dwordx2 v[70:71], v3, s[4:7], s45 offen nt
	buffer_load_dwordx2 v[72:73], v3, s[4:7], s46 offen nt
	buffer_load_dwordx2 v[74:75], v3, s[4:7], s47 offen nt
	ds_write_b128 v5, v[12:15] offset:1536
	ds_write_b128 v5, v[16:19] offset:3584
	s_waitcnt vmcnt(16)
	v_cvt_pkrtz_f16_f32 v12, v92, v94
	v_cvt_pkrtz_f16_f32 v13, v96, v98
	v_cvt_pkrtz_f16_f32 v14, v100, v102
	v_cvt_pkrtz_f16_f32 v15, v104, v106
	v_cvt_pkrtz_f16_f32 v16, v93, v95
	v_cvt_pkrtz_f16_f32 v17, v97, v99
	v_cvt_pkrtz_f16_f32 v18, v101, v103
	v_cvt_pkrtz_f16_f32 v19, v105, v107
	s_mov_b32 s40, 0x22b940
	s_mov_b32 s41, 0x24d5d0
	s_mov_b32 s42, 0x26f260
	s_mov_b32 s43, 0x290ef0
	s_mov_b32 s44, 0x2b2b80
	s_mov_b32 s45, 0x2d4810
	s_mov_b32 s46, 0x2f64a0
	s_mov_b32 s47, 0x318130
	buffer_load_dwordx2 v[76:77], v3, s[4:7], s40 offen nt
	buffer_load_dwordx2 v[78:79], v3, s[4:7], s41 offen nt
	buffer_load_dwordx2 v[80:81], v3, s[4:7], s42 offen nt
	buffer_load_dwordx2 v[82:83], v3, s[4:7], s43 offen nt
	buffer_load_dwordx2 v[84:85], v3, s[4:7], s44 offen nt
	buffer_load_dwordx2 v[86:87], v3, s[4:7], s45 offen nt
	buffer_load_dwordx2 v[88:89], v3, s[4:7], s46 offen nt
	buffer_load_dwordx2 v[90:91], v3, s[4:7], s47 offen nt
	ds_write_b128 v5, v[12:15] offset:1792
	ds_write_b128 v5, v[16:19] offset:3840
	s_waitcnt lgkmcnt(0)
	s_barrier
	ds_write_b128 v254, v[108:111] offset:0
	ds_write_b128 v254, v[112:115] offset:1024
	s_waitcnt lgkmcnt(0)
	s_barrier
	ds_read_b128 v[140:143], v255 offset:0
	ds_read_b128 v[144:147], v255 offset:1024
	ds_read_b128 v[12:15], v6 offset:1024
	ds_read_b128 v[16:19], v6 offset:3072
	ds_read_b128 v[20:23], v7 offset:1024
	ds_read_b128 v[24:27], v7 offset:3072
	ds_read_b128 v[28:31], v8 offset:1024
	ds_read_b128 v[32:35], v8 offset:3072
	ds_read_b128 v[36:39], v9 offset:1024
	ds_read_b128 v[40:43], v9 offset:3072
	s_waitcnt lgkmcnt(7)
	v_mfma_f32_16x16x32_f16 v[188:191], v[148:151], v[12:15], v[188:191]
	v_mfma_f32_16x16x32_f16 v[220:223], v[108:111], v[12:15], v[220:223]
	s_waitcnt lgkmcnt(6)
	v_mfma_f32_16x16x32_f16 v[192:195], v[152:155], v[16:19], v[192:195]
	v_mfma_f32_16x16x32_f16 v[224:227], v[112:115], v[16:19], v[224:227]
	s_waitcnt lgkmcnt(5)
	v_mfma_f32_16x16x32_f16 v[196:199], v[156:159], v[20:23], v[196:199]
	v_mfma_f32_16x16x32_f16 v[228:231], v[116:119], v[20:23], v[228:231]
	s_waitcnt lgkmcnt(4)
	v_mfma_f32_16x16x32_f16 v[200:203], v[160:163], v[24:27], v[200:203]
	v_mfma_f32_16x16x32_f16 v[232:235], v[120:123], v[24:27], v[232:235]
	s_waitcnt lgkmcnt(3)
	v_mfma_f32_16x16x32_f16 v[204:207], v[164:167], v[28:31], v[204:207]
	v_mfma_f32_16x16x32_f16 v[236:239], v[124:127], v[28:31], v[236:239]
	s_waitcnt lgkmcnt(2)
	v_mfma_f32_16x16x32_f16 v[208:211], v[168:171], v[32:35], v[208:211]
	v_mfma_f32_16x16x32_f16 v[240:243], v[128:131], v[32:35], v[240:243]
	s_waitcnt lgkmcnt(1)
	v_mfma_f32_16x16x32_f16 v[212:215], v[172:175], v[36:39], v[212:215]
	v_mfma_f32_16x16x32_f16 v[244:247], v[132:135], v[36:39], v[244:247]
	s_waitcnt lgkmcnt(0)
	v_mfma_f32_16x16x32_f16 v[216:219], v[176:179], v[40:43], v[216:219]
	v_mfma_f32_16x16x32_f16 v[248:251], v[136:139], v[40:43], v[248:251]
	s_mov_b32 s40, 0x339dc0
	s_mov_b32 s41, 0x35ba50
	s_mov_b32 s42, 0x37d6e0
	s_mov_b32 s43, 0x39f370
	s_mov_b32 s44, 0x3c1000
	s_mov_b32 s45, 0x3e2c90
	s_mov_b32 s46, 0x404920
	s_mov_b32 s47, 0x4265b0
	buffer_load_dwordx2 v[92:93], v3, s[4:7], s40 offen nt
	buffer_load_dwordx2 v[94:95], v3, s[4:7], s41 offen nt
	buffer_load_dwordx2 v[96:97], v3, s[4:7], s42 offen nt
	buffer_load_dwordx2 v[98:99], v3, s[4:7], s43 offen nt
	buffer_load_dwordx2 v[100:101], v3, s[4:7], s44 offen nt
	buffer_load_dwordx2 v[102:103], v3, s[4:7], s45 offen nt
	buffer_load_dwordx2 v[104:105], v3, s[4:7], s46 offen nt
	buffer_load_dwordx2 v[106:107], v3, s[4:7], s47 offen nt
	s_waitcnt vmcnt(24)
	v_cvt_pkrtz_f16_f32 v12, v44, v46
	v_cvt_pkrtz_f16_f32 v13, v48, v50
	v_cvt_pkrtz_f16_f32 v14, v52, v54
	v_cvt_pkrtz_f16_f32 v15, v56, v58
	v_cvt_pkrtz_f16_f32 v16, v45, v47
	v_cvt_pkrtz_f16_f32 v17, v49, v51
	v_cvt_pkrtz_f16_f32 v18, v53, v55
	v_cvt_pkrtz_f16_f32 v19, v57, v59
	ds_write_b128 v5, v[12:15] offset:0
	ds_write_b128 v5, v[16:19] offset:2048
	s_waitcnt vmcnt(16)
	v_cvt_pkrtz_f16_f32 v12, v60, v62
	v_cvt_pkrtz_f16_f32 v13, v64, v66
	v_cvt_pkrtz_f16_f32 v14, v68, v70
	v_cvt_pkrtz_f16_f32 v15, v72, v74
	v_cvt_pkrtz_f16_f32 v16, v61, v63
	v_cvt_pkrtz_f16_f32 v17, v65, v67
	v_cvt_pkrtz_f16_f32 v18, v69, v71
	v_cvt_pkrtz_f16_f32 v19, v73, v75
	s_mov_b32 s40, 0x12c50
	s_mov_b32 s41, 0x348e0
	s_mov_b32 s42, 0x56570
	s_mov_b32 s43, 0x78200
	s_mov_b32 s44, 0x99e90
	s_mov_b32 s45, 0xbbb20
	s_mov_b32 s46, 0xdd7b0
	s_mov_b32 s47, 0xff440
	buffer_load_dwordx2 v[44:45], v3, s[4:7], s40 offen nt
	buffer_load_dwordx2 v[46:47], v3, s[4:7], s41 offen nt
	buffer_load_dwordx2 v[48:49], v3, s[4:7], s42 offen nt
	buffer_load_dwordx2 v[50:51], v3, s[4:7], s43 offen nt
	buffer_load_dwordx2 v[52:53], v3, s[4:7], s44 offen nt
	buffer_load_dwordx2 v[54:55], v3, s[4:7], s45 offen nt
	buffer_load_dwordx2 v[56:57], v3, s[4:7], s46 offen nt
	buffer_load_dwordx2 v[58:59], v3, s[4:7], s47 offen nt
	ds_write_b128 v5, v[12:15] offset:256
	ds_write_b128 v5, v[16:19] offset:2304
	s_waitcnt vmcnt(16)
	v_cvt_pkrtz_f16_f32 v12, v76, v78
	v_cvt_pkrtz_f16_f32 v13, v80, v82
	v_cvt_pkrtz_f16_f32 v14, v84, v86
	v_cvt_pkrtz_f16_f32 v15, v88, v90
	v_cvt_pkrtz_f16_f32 v16, v77, v79
	v_cvt_pkrtz_f16_f32 v17, v81, v83
	v_cvt_pkrtz_f16_f32 v18, v85, v87
	v_cvt_pkrtz_f16_f32 v19, v89, v91
	s_mov_b32 s40, 0x1210d0
	s_mov_b32 s41, 0x142d60
	s_mov_b32 s42, 0x1649f0
	s_mov_b32 s43, 0x186680
	s_mov_b32 s44, 0x1a8310
	s_mov_b32 s45, 0x1c9fa0
	s_mov_b32 s46, 0x1ebc30
	s_mov_b32 s47, 0x20d8c0
	buffer_load_dwordx2 v[60:61], v3, s[4:7], s40 offen nt
	buffer_load_dwordx2 v[62:63], v3, s[4:7], s41 offen nt
	buffer_load_dwordx2 v[64:65], v3, s[4:7], s42 offen nt
	buffer_load_dwordx2 v[66:67], v3, s[4:7], s43 offen nt
	buffer_load_dwordx2 v[68:69], v3, s[4:7], s44 offen nt
	buffer_load_dwordx2 v[70:71], v3, s[4:7], s45 offen nt
	buffer_load_dwordx2 v[72:73], v3, s[4:7], s46 offen nt
	buffer_load_dwordx2 v[74:75], v3, s[4:7], s47 offen nt
	ds_write_b128 v5, v[12:15] offset:512
	ds_write_b128 v5, v[16:19] offset:2560
	s_waitcnt vmcnt(16)
	v_cvt_pkrtz_f16_f32 v12, v92, v94
	v_cvt_pkrtz_f16_f32 v13, v96, v98
	v_cvt_pkrtz_f16_f32 v14, v100, v102
	v_cvt_pkrtz_f16_f32 v15, v104, v106
	v_cvt_pkrtz_f16_f32 v16, v93, v95
	v_cvt_pkrtz_f16_f32 v17, v97, v99
	v_cvt_pkrtz_f16_f32 v18, v101, v103
	v_cvt_pkrtz_f16_f32 v19, v105, v107
	s_mov_b32 s40, 0x22f550
	s_mov_b32 s41, 0x2511e0
	s_mov_b32 s42, 0x272e70
	s_mov_b32 s43, 0x294b00
	s_mov_b32 s44, 0x2b6790
	s_mov_b32 s45, 0x2d8420
	s_mov_b32 s46, 0x2fa0b0
	s_mov_b32 s47, 0x31bd40
	buffer_load_dwordx2 v[76:77], v3, s[4:7], s40 offen nt
	buffer_load_dwordx2 v[78:79], v3, s[4:7], s41 offen nt
	buffer_load_dwordx2 v[80:81], v3, s[4:7], s42 offen nt
	buffer_load_dwordx2 v[82:83], v3, s[4:7], s43 offen nt
	buffer_load_dwordx2 v[84:85], v3, s[4:7], s44 offen nt
	buffer_load_dwordx2 v[86:87], v3, s[4:7], s45 offen nt
	buffer_load_dwordx2 v[88:89], v3, s[4:7], s46 offen nt
	buffer_load_dwordx2 v[90:91], v3, s[4:7], s47 offen nt
	ds_write_b128 v5, v[12:15] offset:768
	ds_write_b128 v5, v[16:19] offset:2816
	s_waitcnt lgkmcnt(0)
	s_barrier
	ds_read_b128 v[12:15], v6 offset:0
	ds_read_b128 v[16:19], v6 offset:2048
	ds_read_b128 v[20:23], v7 offset:0
	ds_read_b128 v[24:27], v7 offset:2048
	ds_read_b128 v[28:31], v8 offset:0
	ds_read_b128 v[32:35], v8 offset:2048
	ds_read_b128 v[36:39], v9 offset:0
	ds_read_b128 v[40:43], v9 offset:2048
	s_waitcnt lgkmcnt(7)
	v_mfma_f32_16x16x32_f16 v[188:191], v[152:155], v[12:15], v[188:191]
	v_mfma_f32_16x16x32_f16 v[220:223], v[112:115], v[12:15], v[220:223]
	s_waitcnt lgkmcnt(6)
	v_mfma_f32_16x16x32_f16 v[192:195], v[156:159], v[16:19], v[192:195]
	v_mfma_f32_16x16x32_f16 v[224:227], v[116:119], v[16:19], v[224:227]
	s_waitcnt lgkmcnt(5)
	v_mfma_f32_16x16x32_f16 v[196:199], v[160:163], v[20:23], v[196:199]
	v_mfma_f32_16x16x32_f16 v[228:231], v[120:123], v[20:23], v[228:231]
	s_waitcnt lgkmcnt(4)
	v_mfma_f32_16x16x32_f16 v[200:203], v[164:167], v[24:27], v[200:203]
	v_mfma_f32_16x16x32_f16 v[232:235], v[124:127], v[24:27], v[232:235]
	s_waitcnt lgkmcnt(3)
	v_mfma_f32_16x16x32_f16 v[204:207], v[168:171], v[28:31], v[204:207]
	v_mfma_f32_16x16x32_f16 v[236:239], v[128:131], v[28:31], v[236:239]
	s_waitcnt lgkmcnt(2)
	v_mfma_f32_16x16x32_f16 v[208:211], v[172:175], v[32:35], v[208:211]
	v_mfma_f32_16x16x32_f16 v[240:243], v[132:135], v[32:35], v[240:243]
	s_waitcnt lgkmcnt(1)
	v_mfma_f32_16x16x32_f16 v[212:215], v[176:179], v[36:39], v[212:215]
	v_mfma_f32_16x16x32_f16 v[244:247], v[136:139], v[36:39], v[244:247]
	s_waitcnt lgkmcnt(0)
	v_mfma_f32_16x16x32_f16 v[216:219], v[180:183], v[40:43], v[216:219]
	v_mfma_f32_16x16x32_f16 v[248:251], v[140:143], v[40:43], v[248:251]
	s_mov_b32 s40, 0x33d9d0
	s_mov_b32 s41, 0x35f660
	s_mov_b32 s42, 0x3812f0
	s_mov_b32 s43, 0x3a2f80
	s_mov_b32 s44, 0x3c4c10
	s_mov_b32 s45, 0x3e68a0
	s_mov_b32 s46, 0x408530
	s_mov_b32 s47, 0x42a1c0
	buffer_load_dwordx2 v[92:93], v3, s[4:7], s40 offen nt
	buffer_load_dwordx2 v[94:95], v3, s[4:7], s41 offen nt
	buffer_load_dwordx2 v[96:97], v3, s[4:7], s42 offen nt
	buffer_load_dwordx2 v[98:99], v3, s[4:7], s43 offen nt
	buffer_load_dwordx2 v[100:101], v3, s[4:7], s44 offen nt
	buffer_load_dwordx2 v[102:103], v3, s[4:7], s45 offen nt
	buffer_load_dwordx2 v[104:105], v3, s[4:7], s46 offen nt
	buffer_load_dwordx2 v[106:107], v3, s[4:7], s47 offen nt
	s_waitcnt vmcnt(24)
	v_cvt_pkrtz_f16_f32 v12, v44, v46
	v_cvt_pkrtz_f16_f32 v13, v48, v50
	v_cvt_pkrtz_f16_f32 v14, v52, v54
	v_cvt_pkrtz_f16_f32 v15, v56, v58
	v_cvt_pkrtz_f16_f32 v16, v45, v47
	v_cvt_pkrtz_f16_f32 v17, v49, v51
	v_cvt_pkrtz_f16_f32 v18, v53, v55
	v_cvt_pkrtz_f16_f32 v19, v57, v59
	ds_write_b128 v5, v[12:15] offset:1024
	ds_write_b128 v5, v[16:19] offset:3072
	s_waitcnt vmcnt(16)
	v_cvt_pkrtz_f16_f32 v12, v60, v62
	v_cvt_pkrtz_f16_f32 v13, v64, v66
	v_cvt_pkrtz_f16_f32 v14, v68, v70
	v_cvt_pkrtz_f16_f32 v15, v72, v74
	v_cvt_pkrtz_f16_f32 v16, v61, v63
	v_cvt_pkrtz_f16_f32 v17, v65, v67
	v_cvt_pkrtz_f16_f32 v18, v69, v71
	v_cvt_pkrtz_f16_f32 v19, v73, v75
	s_mov_b32 s40, 0x16860
	s_mov_b32 s41, 0x384f0
	s_mov_b32 s42, 0x5a180
	s_mov_b32 s43, 0x7be10
	s_mov_b32 s44, 0x9daa0
	s_mov_b32 s45, 0xbf730
	s_mov_b32 s46, 0xe13c0
	s_mov_b32 s47, 0x103050
	buffer_load_dwordx2 v[44:45], v3, s[4:7], s40 offen nt
	buffer_load_dwordx2 v[46:47], v3, s[4:7], s41 offen nt
	buffer_load_dwordx2 v[48:49], v3, s[4:7], s42 offen nt
	buffer_load_dwordx2 v[50:51], v3, s[4:7], s43 offen nt
	buffer_load_dwordx2 v[52:53], v3, s[4:7], s44 offen nt
	buffer_load_dwordx2 v[54:55], v3, s[4:7], s45 offen nt
	buffer_load_dwordx2 v[56:57], v3, s[4:7], s46 offen nt
	buffer_load_dwordx2 v[58:59], v3, s[4:7], s47 offen nt
	ds_write_b128 v5, v[12:15] offset:1280
	ds_write_b128 v5, v[16:19] offset:3328
	s_waitcnt vmcnt(16)
	v_cvt_pkrtz_f16_f32 v12, v76, v78
	v_cvt_pkrtz_f16_f32 v13, v80, v82
	v_cvt_pkrtz_f16_f32 v14, v84, v86
	v_cvt_pkrtz_f16_f32 v15, v88, v90
	v_cvt_pkrtz_f16_f32 v16, v77, v79
	v_cvt_pkrtz_f16_f32 v17, v81, v83
	v_cvt_pkrtz_f16_f32 v18, v85, v87
	v_cvt_pkrtz_f16_f32 v19, v89, v91
	s_mov_b32 s40, 0x124ce0
	s_mov_b32 s41, 0x146970
	s_mov_b32 s42, 0x168600
	s_mov_b32 s43, 0x18a290
	s_mov_b32 s44, 0x1abf20
	s_mov_b32 s45, 0x1cdbb0
	s_mov_b32 s46, 0x1ef840
	s_mov_b32 s47, 0x2114d0
	buffer_load_dwordx2 v[60:61], v3, s[4:7], s40 offen nt
	buffer_load_dwordx2 v[62:63], v3, s[4:7], s41 offen nt
	buffer_load_dwordx2 v[64:65], v3, s[4:7], s42 offen nt
	buffer_load_dwordx2 v[66:67], v3, s[4:7], s43 offen nt
	buffer_load_dwordx2 v[68:69], v3, s[4:7], s44 offen nt
	buffer_load_dwordx2 v[70:71], v3, s[4:7], s45 offen nt
	buffer_load_dwordx2 v[72:73], v3, s[4:7], s46 offen nt
	buffer_load_dwordx2 v[74:75], v3, s[4:7], s47 offen nt
	ds_write_b128 v5, v[12:15] offset:1536
	ds_write_b128 v5, v[16:19] offset:3584
	s_waitcnt vmcnt(16)
	v_cvt_pkrtz_f16_f32 v12, v92, v94
	v_cvt_pkrtz_f16_f32 v13, v96, v98
	v_cvt_pkrtz_f16_f32 v14, v100, v102
	v_cvt_pkrtz_f16_f32 v15, v104, v106
	v_cvt_pkrtz_f16_f32 v16, v93, v95
	v_cvt_pkrtz_f16_f32 v17, v97, v99
	v_cvt_pkrtz_f16_f32 v18, v101, v103
	v_cvt_pkrtz_f16_f32 v19, v105, v107
	s_mov_b32 s40, 0x233160
	s_mov_b32 s41, 0x254df0
	s_mov_b32 s42, 0x276a80
	s_mov_b32 s43, 0x298710
	s_mov_b32 s44, 0x2ba3a0
	s_mov_b32 s45, 0x2dc030
	s_mov_b32 s46, 0x2fdcc0
	s_mov_b32 s47, 0x31f950
	buffer_load_dwordx2 v[76:77], v3, s[4:7], s40 offen nt
	buffer_load_dwordx2 v[78:79], v3, s[4:7], s41 offen nt
	buffer_load_dwordx2 v[80:81], v3, s[4:7], s42 offen nt
	buffer_load_dwordx2 v[82:83], v3, s[4:7], s43 offen nt
	buffer_load_dwordx2 v[84:85], v3, s[4:7], s44 offen nt
	buffer_load_dwordx2 v[86:87], v3, s[4:7], s45 offen nt
	buffer_load_dwordx2 v[88:89], v3, s[4:7], s46 offen nt
	buffer_load_dwordx2 v[90:91], v3, s[4:7], s47 offen nt
	ds_write_b128 v5, v[12:15] offset:1792
	ds_write_b128 v5, v[16:19] offset:3840
	s_waitcnt lgkmcnt(0)
	s_barrier
	ds_read_b128 v[12:15], v6 offset:1024
	ds_read_b128 v[16:19], v6 offset:3072
	ds_read_b128 v[20:23], v7 offset:1024
	ds_read_b128 v[24:27], v7 offset:3072
	ds_read_b128 v[28:31], v8 offset:1024
	ds_read_b128 v[32:35], v8 offset:3072
	ds_read_b128 v[36:39], v9 offset:1024
	ds_read_b128 v[40:43], v9 offset:3072
	s_waitcnt lgkmcnt(7)
	v_mfma_f32_16x16x32_f16 v[188:191], v[156:159], v[12:15], v[188:191]
	v_mfma_f32_16x16x32_f16 v[220:223], v[116:119], v[12:15], v[220:223]
	s_waitcnt lgkmcnt(6)
	v_mfma_f32_16x16x32_f16 v[192:195], v[160:163], v[16:19], v[192:195]
	v_mfma_f32_16x16x32_f16 v[224:227], v[120:123], v[16:19], v[224:227]
	s_waitcnt lgkmcnt(5)
	v_mfma_f32_16x16x32_f16 v[196:199], v[164:167], v[20:23], v[196:199]
	v_mfma_f32_16x16x32_f16 v[228:231], v[124:127], v[20:23], v[228:231]
	s_waitcnt lgkmcnt(4)
	v_mfma_f32_16x16x32_f16 v[200:203], v[168:171], v[24:27], v[200:203]
	v_mfma_f32_16x16x32_f16 v[232:235], v[128:131], v[24:27], v[232:235]
	s_waitcnt lgkmcnt(3)
	v_mfma_f32_16x16x32_f16 v[204:207], v[172:175], v[28:31], v[204:207]
	v_mfma_f32_16x16x32_f16 v[236:239], v[132:135], v[28:31], v[236:239]
	s_waitcnt lgkmcnt(2)
	v_mfma_f32_16x16x32_f16 v[208:211], v[176:179], v[32:35], v[208:211]
	v_mfma_f32_16x16x32_f16 v[240:243], v[136:139], v[32:35], v[240:243]
	s_waitcnt lgkmcnt(1)
	v_mfma_f32_16x16x32_f16 v[212:215], v[180:183], v[36:39], v[212:215]
	v_mfma_f32_16x16x32_f16 v[244:247], v[140:143], v[36:39], v[244:247]
	s_waitcnt lgkmcnt(0)
	v_mfma_f32_16x16x32_f16 v[216:219], v[184:187], v[40:43], v[216:219]
	v_mfma_f32_16x16x32_f16 v[248:251], v[144:147], v[40:43], v[248:251]
	s_mov_b32 s40, 0x30000
	s_mov_b32 s41, 0x30400
	s_mov_b32 s42, 0x30800
	s_mov_b32 s43, 0x30c00
	buffer_load_dwordx4 v[148:151], v4, s[8:11], s40 offen
	buffer_load_dwordx4 v[152:155], v4, s[8:11], s41 offen
	buffer_load_dwordx4 v[156:159], v4, s[8:11], s42 offen
	buffer_load_dwordx4 v[160:163], v4, s[8:11], s43 offen
	s_mov_b32 s40, 0x31000
	s_mov_b32 s41, 0x31400
	s_mov_b32 s42, 0x31800
	s_mov_b32 s43, 0x31c00
	buffer_load_dwordx4 v[164:167], v4, s[8:11], s40 offen
	buffer_load_dwordx4 v[168:171], v4, s[8:11], s41 offen
	buffer_load_dwordx4 v[172:175], v4, s[8:11], s42 offen
	buffer_load_dwordx4 v[176:179], v4, s[8:11], s43 offen
	s_mov_b32 s40, 0x3415e0
	s_mov_b32 s41, 0x363270
	s_mov_b32 s42, 0x384f00
	s_mov_b32 s43, 0x3a6b90
	s_mov_b32 s44, 0x3c8820
	s_mov_b32 s45, 0x3ea4b0
	s_mov_b32 s46, 0x40c140
	s_mov_b32 s47, 0x42ddd0
	buffer_load_dwordx2 v[92:93], v3, s[4:7], s40 offen nt
	buffer_load_dwordx2 v[94:95], v3, s[4:7], s41 offen nt
	buffer_load_dwordx2 v[96:97], v3, s[4:7], s42 offen nt
	buffer_load_dwordx2 v[98:99], v3, s[4:7], s43 offen nt
	buffer_load_dwordx2 v[100:101], v3, s[4:7], s44 offen nt
	buffer_load_dwordx2 v[102:103], v3, s[4:7], s45 offen nt
	buffer_load_dwordx2 v[104:105], v3, s[4:7], s46 offen nt
	buffer_load_dwordx2 v[106:107], v3, s[4:7], s47 offen nt
	s_waitcnt vmcnt(32)
	v_cvt_pkrtz_f16_f32 v12, v44, v46
	v_cvt_pkrtz_f16_f32 v13, v48, v50
	v_cvt_pkrtz_f16_f32 v14, v52, v54
	v_cvt_pkrtz_f16_f32 v15, v56, v58
	v_cvt_pkrtz_f16_f32 v16, v45, v47
	v_cvt_pkrtz_f16_f32 v17, v49, v51
	v_cvt_pkrtz_f16_f32 v18, v53, v55
	v_cvt_pkrtz_f16_f32 v19, v57, v59
	ds_write_b128 v5, v[12:15] offset:0
	ds_write_b128 v5, v[16:19] offset:2048
	s_waitcnt vmcnt(24)
	v_cvt_pkrtz_f16_f32 v12, v60, v62
	v_cvt_pkrtz_f16_f32 v13, v64, v66
	v_cvt_pkrtz_f16_f32 v14, v68, v70
	v_cvt_pkrtz_f16_f32 v15, v72, v74
	v_cvt_pkrtz_f16_f32 v16, v61, v63
	v_cvt_pkrtz_f16_f32 v17, v65, v67
	v_cvt_pkrtz_f16_f32 v18, v69, v71
	v_cvt_pkrtz_f16_f32 v19, v73, v75
	s_mov_b32 s40, 0x1a470
	s_mov_b32 s41, 0x3c100
	s_mov_b32 s42, 0x5dd90
	s_mov_b32 s43, 0x7fa20
	s_mov_b32 s44, 0xa16b0
	s_mov_b32 s45, 0xc3340
	s_mov_b32 s46, 0xe4fd0
	s_mov_b32 s47, 0x106c60
	buffer_load_dwordx2 v[44:45], v3, s[4:7], s40 offen nt
	buffer_load_dwordx2 v[46:47], v3, s[4:7], s41 offen nt
	buffer_load_dwordx2 v[48:49], v3, s[4:7], s42 offen nt
	buffer_load_dwordx2 v[50:51], v3, s[4:7], s43 offen nt
	buffer_load_dwordx2 v[52:53], v3, s[4:7], s44 offen nt
	buffer_load_dwordx2 v[54:55], v3, s[4:7], s45 offen nt
	buffer_load_dwordx2 v[56:57], v3, s[4:7], s46 offen nt
	buffer_load_dwordx2 v[58:59], v3, s[4:7], s47 offen nt
	ds_write_b128 v5, v[12:15] offset:256
	ds_write_b128 v5, v[16:19] offset:2304
	s_waitcnt vmcnt(24)
	v_cvt_pkrtz_f16_f32 v12, v76, v78
	v_cvt_pkrtz_f16_f32 v13, v80, v82
	v_cvt_pkrtz_f16_f32 v14, v84, v86
	v_cvt_pkrtz_f16_f32 v15, v88, v90
	v_cvt_pkrtz_f16_f32 v16, v77, v79
	v_cvt_pkrtz_f16_f32 v17, v81, v83
	v_cvt_pkrtz_f16_f32 v18, v85, v87
	v_cvt_pkrtz_f16_f32 v19, v89, v91
	s_mov_b32 s40, 0x1288f0
	s_mov_b32 s41, 0x14a580
	s_mov_b32 s42, 0x16c210
	s_mov_b32 s43, 0x18dea0
	s_mov_b32 s44, 0x1afb30
	s_mov_b32 s45, 0x1d17c0
	s_mov_b32 s46, 0x1f3450
	s_mov_b32 s47, 0x2150e0
	buffer_load_dwordx2 v[60:61], v3, s[4:7], s40 offen nt
	buffer_load_dwordx2 v[62:63], v3, s[4:7], s41 offen nt
	buffer_load_dwordx2 v[64:65], v3, s[4:7], s42 offen nt
	buffer_load_dwordx2 v[66:67], v3, s[4:7], s43 offen nt
	buffer_load_dwordx2 v[68:69], v3, s[4:7], s44 offen nt
	buffer_load_dwordx2 v[70:71], v3, s[4:7], s45 offen nt
	buffer_load_dwordx2 v[72:73], v3, s[4:7], s46 offen nt
	buffer_load_dwordx2 v[74:75], v3, s[4:7], s47 offen nt
	ds_write_b128 v5, v[12:15] offset:512
	ds_write_b128 v5, v[16:19] offset:2560
	s_waitcnt vmcnt(16)
	v_cvt_pkrtz_f16_f32 v12, v92, v94
	v_cvt_pkrtz_f16_f32 v13, v96, v98
	v_cvt_pkrtz_f16_f32 v14, v100, v102
	v_cvt_pkrtz_f16_f32 v15, v104, v106
	v_cvt_pkrtz_f16_f32 v16, v93, v95
	v_cvt_pkrtz_f16_f32 v17, v97, v99
	v_cvt_pkrtz_f16_f32 v18, v101, v103
	v_cvt_pkrtz_f16_f32 v19, v105, v107
	s_mov_b32 s40, 0x236d70
	s_mov_b32 s41, 0x258a00
	s_mov_b32 s42, 0x27a690
	s_mov_b32 s43, 0x29c320
	s_mov_b32 s44, 0x2bdfb0
	s_mov_b32 s45, 0x2dfc40
	s_mov_b32 s46, 0x3018d0
	s_mov_b32 s47, 0x323560
	buffer_load_dwordx2 v[76:77], v3, s[4:7], s40 offen nt
	buffer_load_dwordx2 v[78:79], v3, s[4:7], s41 offen nt
	buffer_load_dwordx2 v[80:81], v3, s[4:7], s42 offen nt
	buffer_load_dwordx2 v[82:83], v3, s[4:7], s43 offen nt
	buffer_load_dwordx2 v[84:85], v3, s[4:7], s44 offen nt
	buffer_load_dwordx2 v[86:87], v3, s[4:7], s45 offen nt
	buffer_load_dwordx2 v[88:89], v3, s[4:7], s46 offen nt
	buffer_load_dwordx2 v[90:91], v3, s[4:7], s47 offen nt
	ds_write_b128 v5, v[12:15] offset:768
	ds_write_b128 v5, v[16:19] offset:2816
	s_waitcnt lgkmcnt(0)
	s_barrier
	ds_write_b128 v254, v[148:151] offset:16384
	ds_write_b128 v254, v[152:155] offset:17408
	s_waitcnt lgkmcnt(0)
	s_barrier
	ds_read_b128 v[180:183], v255 offset:16384
	ds_read_b128 v[184:187], v255 offset:17408
	ds_read_b128 v[12:15], v6 offset:0
	ds_read_b128 v[16:19], v6 offset:2048
	ds_read_b128 v[20:23], v7 offset:0
	ds_read_b128 v[24:27], v7 offset:2048
	ds_read_b128 v[28:31], v8 offset:0
	ds_read_b128 v[32:35], v8 offset:2048
	ds_read_b128 v[36:39], v9 offset:0
	ds_read_b128 v[40:43], v9 offset:2048
	s_waitcnt lgkmcnt(7)
	v_mfma_f32_16x16x32_f16 v[188:191], v[108:111], v[12:15], v[188:191]
	v_mfma_f32_16x16x32_f16 v[220:223], v[148:151], v[12:15], v[220:223]
	s_waitcnt lgkmcnt(6)
	v_mfma_f32_16x16x32_f16 v[192:195], v[112:115], v[16:19], v[192:195]
	v_mfma_f32_16x16x32_f16 v[224:227], v[152:155], v[16:19], v[224:227]
	s_waitcnt lgkmcnt(5)
	v_mfma_f32_16x16x32_f16 v[196:199], v[116:119], v[20:23], v[196:199]
	v_mfma_f32_16x16x32_f16 v[228:231], v[156:159], v[20:23], v[228:231]
	s_waitcnt lgkmcnt(4)
	v_mfma_f32_16x16x32_f16 v[200:203], v[120:123], v[24:27], v[200:203]
	v_mfma_f32_16x16x32_f16 v[232:235], v[160:163], v[24:27], v[232:235]
	s_waitcnt lgkmcnt(3)
	v_mfma_f32_16x16x32_f16 v[204:207], v[124:127], v[28:31], v[204:207]
	v_mfma_f32_16x16x32_f16 v[236:239], v[164:167], v[28:31], v[236:239]
	s_waitcnt lgkmcnt(2)
	v_mfma_f32_16x16x32_f16 v[208:211], v[128:131], v[32:35], v[208:211]
	v_mfma_f32_16x16x32_f16 v[240:243], v[168:171], v[32:35], v[240:243]
	s_waitcnt lgkmcnt(1)
	v_mfma_f32_16x16x32_f16 v[212:215], v[132:135], v[36:39], v[212:215]
	v_mfma_f32_16x16x32_f16 v[244:247], v[172:175], v[36:39], v[244:247]
	s_waitcnt lgkmcnt(0)
	v_mfma_f32_16x16x32_f16 v[216:219], v[136:139], v[40:43], v[216:219]
	v_mfma_f32_16x16x32_f16 v[248:251], v[176:179], v[40:43], v[248:251]
	s_mov_b32 s40, 0x3451f0
	s_mov_b32 s41, 0x366e80
	s_mov_b32 s42, 0x388b10
	s_mov_b32 s43, 0x3aa7a0
	s_mov_b32 s44, 0x3cc430
	s_mov_b32 s45, 0x3ee0c0
	s_mov_b32 s46, 0x40fd50
	s_mov_b32 s47, 0x4319e0
	buffer_load_dwordx2 v[92:93], v3, s[4:7], s40 offen nt
	buffer_load_dwordx2 v[94:95], v3, s[4:7], s41 offen nt
	buffer_load_dwordx2 v[96:97], v3, s[4:7], s42 offen nt
	buffer_load_dwordx2 v[98:99], v3, s[4:7], s43 offen nt
	buffer_load_dwordx2 v[100:101], v3, s[4:7], s44 offen nt
	buffer_load_dwordx2 v[102:103], v3, s[4:7], s45 offen nt
	buffer_load_dwordx2 v[104:105], v3, s[4:7], s46 offen nt
	buffer_load_dwordx2 v[106:107], v3, s[4:7], s47 offen nt
	s_waitcnt vmcnt(24)
	v_cvt_pkrtz_f16_f32 v12, v44, v46
	v_cvt_pkrtz_f16_f32 v13, v48, v50
	v_cvt_pkrtz_f16_f32 v14, v52, v54
	v_cvt_pkrtz_f16_f32 v15, v56, v58
	v_cvt_pkrtz_f16_f32 v16, v45, v47
	v_cvt_pkrtz_f16_f32 v17, v49, v51
	v_cvt_pkrtz_f16_f32 v18, v53, v55
	v_cvt_pkrtz_f16_f32 v19, v57, v59
	ds_write_b128 v5, v[12:15] offset:1024
	ds_write_b128 v5, v[16:19] offset:3072
	s_waitcnt vmcnt(16)
	v_cvt_pkrtz_f16_f32 v12, v60, v62
	v_cvt_pkrtz_f16_f32 v13, v64, v66
	v_cvt_pkrtz_f16_f32 v14, v68, v70
	v_cvt_pkrtz_f16_f32 v15, v72, v74
	v_cvt_pkrtz_f16_f32 v16, v61, v63
	v_cvt_pkrtz_f16_f32 v17, v65, v67
	v_cvt_pkrtz_f16_f32 v18, v69, v71
	v_cvt_pkrtz_f16_f32 v19, v73, v75
	s_mov_b32 s40, 0x1e080
	s_mov_b32 s41, 0x3fd10
	s_mov_b32 s42, 0x619a0
	s_mov_b32 s43, 0x83630
	s_mov_b32 s44, 0xa52c0
	s_mov_b32 s45, 0xc6f50
	s_mov_b32 s46, 0xe8be0
	s_mov_b32 s47, 0x10a870
	buffer_load_dwordx2 v[44:45], v3, s[4:7], s40 offen nt
	buffer_load_dwordx2 v[46:47], v3, s[4:7], s41 offen nt
	buffer_load_dwordx2 v[48:49], v3, s[4:7], s42 offen nt
	buffer_load_dwordx2 v[50:51], v3, s[4:7], s43 offen nt
	buffer_load_dwordx2 v[52:53], v3, s[4:7], s44 offen nt
	buffer_load_dwordx2 v[54:55], v3, s[4:7], s45 offen nt
	buffer_load_dwordx2 v[56:57], v3, s[4:7], s46 offen nt
	buffer_load_dwordx2 v[58:59], v3, s[4:7], s47 offen nt
	ds_write_b128 v5, v[12:15] offset:1280
	ds_write_b128 v5, v[16:19] offset:3328
	s_waitcnt vmcnt(16)
	v_cvt_pkrtz_f16_f32 v12, v76, v78
	v_cvt_pkrtz_f16_f32 v13, v80, v82
	v_cvt_pkrtz_f16_f32 v14, v84, v86
	v_cvt_pkrtz_f16_f32 v15, v88, v90
	v_cvt_pkrtz_f16_f32 v16, v77, v79
	v_cvt_pkrtz_f16_f32 v17, v81, v83
	v_cvt_pkrtz_f16_f32 v18, v85, v87
	v_cvt_pkrtz_f16_f32 v19, v89, v91
	s_mov_b32 s40, 0x12c500
	s_mov_b32 s41, 0x14e190
	s_mov_b32 s42, 0x16fe20
	s_mov_b32 s43, 0x191ab0
	s_mov_b32 s44, 0x1b3740
	s_mov_b32 s45, 0x1d53d0
	s_mov_b32 s46, 0x1f7060
	s_mov_b32 s47, 0x218cf0
	buffer_load_dwordx2 v[60:61], v3, s[4:7], s40 offen nt
	buffer_load_dwordx2 v[62:63], v3, s[4:7], s41 offen nt
	buffer_load_dwordx2 v[64:65], v3, s[4:7], s42 offen nt
	buffer_load_dwordx2 v[66:67], v3, s[4:7], s43 offen nt
	buffer_load_dwordx2 v[68:69], v3, s[4:7], s44 offen nt
	buffer_load_dwordx2 v[70:71], v3, s[4:7], s45 offen nt
	buffer_load_dwordx2 v[72:73], v3, s[4:7], s46 offen nt
	buffer_load_dwordx2 v[74:75], v3, s[4:7], s47 offen nt
	ds_write_b128 v5, v[12:15] offset:1536
	ds_write_b128 v5, v[16:19] offset:3584
	s_waitcnt vmcnt(16)
	v_cvt_pkrtz_f16_f32 v12, v92, v94
	v_cvt_pkrtz_f16_f32 v13, v96, v98
	v_cvt_pkrtz_f16_f32 v14, v100, v102
	v_cvt_pkrtz_f16_f32 v15, v104, v106
	v_cvt_pkrtz_f16_f32 v16, v93, v95
	v_cvt_pkrtz_f16_f32 v17, v97, v99
	v_cvt_pkrtz_f16_f32 v18, v101, v103
	v_cvt_pkrtz_f16_f32 v19, v105, v107
	s_mov_b32 s40, 0x23a980
	s_mov_b32 s41, 0x25c610
	s_mov_b32 s42, 0x27e2a0
	s_mov_b32 s43, 0x29ff30
	s_mov_b32 s44, 0x2c1bc0
	s_mov_b32 s45, 0x2e3850
	s_mov_b32 s46, 0x3054e0
	s_mov_b32 s47, 0x327170
	buffer_load_dwordx2 v[76:77], v3, s[4:7], s40 offen nt
	buffer_load_dwordx2 v[78:79], v3, s[4:7], s41 offen nt
	buffer_load_dwordx2 v[80:81], v3, s[4:7], s42 offen nt
	buffer_load_dwordx2 v[82:83], v3, s[4:7], s43 offen nt
	buffer_load_dwordx2 v[84:85], v3, s[4:7], s44 offen nt
	buffer_load_dwordx2 v[86:87], v3, s[4:7], s45 offen nt
	buffer_load_dwordx2 v[88:89], v3, s[4:7], s46 offen nt
	buffer_load_dwordx2 v[90:91], v3, s[4:7], s47 offen nt
	ds_write_b128 v5, v[12:15] offset:1792
	ds_write_b128 v5, v[16:19] offset:3840
	s_waitcnt lgkmcnt(0)
	s_barrier
	ds_read_b128 v[12:15], v6 offset:1024
	ds_read_b128 v[16:19], v6 offset:3072
	ds_read_b128 v[20:23], v7 offset:1024
	ds_read_b128 v[24:27], v7 offset:3072
	ds_read_b128 v[28:31], v8 offset:1024
	ds_read_b128 v[32:35], v8 offset:3072
	ds_read_b128 v[36:39], v9 offset:1024
	ds_read_b128 v[40:43], v9 offset:3072
	s_waitcnt lgkmcnt(7)
	v_mfma_f32_16x16x32_f16 v[188:191], v[112:115], v[12:15], v[188:191]
	v_mfma_f32_16x16x32_f16 v[220:223], v[152:155], v[12:15], v[220:223]
	s_waitcnt lgkmcnt(6)
	v_mfma_f32_16x16x32_f16 v[192:195], v[116:119], v[16:19], v[192:195]
	v_mfma_f32_16x16x32_f16 v[224:227], v[156:159], v[16:19], v[224:227]
	s_waitcnt lgkmcnt(5)
	v_mfma_f32_16x16x32_f16 v[196:199], v[120:123], v[20:23], v[196:199]
	v_mfma_f32_16x16x32_f16 v[228:231], v[160:163], v[20:23], v[228:231]
	s_waitcnt lgkmcnt(4)
	v_mfma_f32_16x16x32_f16 v[200:203], v[124:127], v[24:27], v[200:203]
	v_mfma_f32_16x16x32_f16 v[232:235], v[164:167], v[24:27], v[232:235]
	s_waitcnt lgkmcnt(3)
	v_mfma_f32_16x16x32_f16 v[204:207], v[128:131], v[28:31], v[204:207]
	v_mfma_f32_16x16x32_f16 v[236:239], v[168:171], v[28:31], v[236:239]
	s_waitcnt lgkmcnt(2)
	v_mfma_f32_16x16x32_f16 v[208:211], v[132:135], v[32:35], v[208:211]
	v_mfma_f32_16x16x32_f16 v[240:243], v[172:175], v[32:35], v[240:243]
	s_waitcnt lgkmcnt(1)
	v_mfma_f32_16x16x32_f16 v[212:215], v[136:139], v[36:39], v[212:215]
	v_mfma_f32_16x16x32_f16 v[244:247], v[176:179], v[36:39], v[244:247]
	s_waitcnt lgkmcnt(0)
	v_mfma_f32_16x16x32_f16 v[216:219], v[140:143], v[40:43], v[216:219]
	v_mfma_f32_16x16x32_f16 v[248:251], v[180:183], v[40:43], v[248:251]
	s_mov_b32 s40, 0x348e00
	s_mov_b32 s41, 0x36aa90
	s_mov_b32 s42, 0x38c720
	s_mov_b32 s43, 0x3ae3b0
	s_mov_b32 s44, 0x3d0040
	s_mov_b32 s45, 0x3f1cd0
	s_mov_b32 s46, 0x413960
	s_mov_b32 s47, 0x4355f0
	buffer_load_dwordx2 v[92:93], v3, s[4:7], s40 offen nt
	buffer_load_dwordx2 v[94:95], v3, s[4:7], s41 offen nt
	buffer_load_dwordx2 v[96:97], v3, s[4:7], s42 offen nt
	buffer_load_dwordx2 v[98:99], v3, s[4:7], s43 offen nt
	buffer_load_dwordx2 v[100:101], v3, s[4:7], s44 offen nt
	buffer_load_dwordx2 v[102:103], v3, s[4:7], s45 offen nt
	buffer_load_dwordx2 v[104:105], v3, s[4:7], s46 offen nt
	buffer_load_dwordx2 v[106:107], v3, s[4:7], s47 offen nt
	s_waitcnt vmcnt(24)
	v_cvt_pkrtz_f16_f32 v12, v44, v46
	v_cvt_pkrtz_f16_f32 v13, v48, v50
	v_cvt_pkrtz_f16_f32 v14, v52, v54
	v_cvt_pkrtz_f16_f32 v15, v56, v58
	v_cvt_pkrtz_f16_f32 v16, v45, v47
	v_cvt_pkrtz_f16_f32 v17, v49, v51
	v_cvt_pkrtz_f16_f32 v18, v53, v55
	v_cvt_pkrtz_f16_f32 v19, v57, v59
	v_lshrrev_b32_e32 v48, 8, v0
	v_mul_u32_u24_e32 v48, 0xf0400, v48
	v_sub_u32_e32 v48, v11, v48
	buffer_load_dwordx4 v[44:47], v48, s[28:31], 0 offen
	ds_write_b128 v5, v[12:15] offset:0
	ds_write_b128 v5, v[16:19] offset:2048
	s_waitcnt vmcnt(17)
	v_cvt_pkrtz_f16_f32 v12, v60, v62
	v_cvt_pkrtz_f16_f32 v13, v64, v66
	v_cvt_pkrtz_f16_f32 v14, v68, v70
	v_cvt_pkrtz_f16_f32 v15, v72, v74
	v_cvt_pkrtz_f16_f32 v16, v61, v63
	v_cvt_pkrtz_f16_f32 v17, v65, v67
	v_cvt_pkrtz_f16_f32 v18, v69, v71
	v_cvt_pkrtz_f16_f32 v19, v73, v75
	ds_write_b128 v5, v[12:15] offset:256
	ds_write_b128 v5, v[16:19] offset:2304
	s_waitcnt vmcnt(9)
	v_cvt_pkrtz_f16_f32 v12, v76, v78
	v_cvt_pkrtz_f16_f32 v13, v80, v82
	v_cvt_pkrtz_f16_f32 v14, v84, v86
	v_cvt_pkrtz_f16_f32 v15, v88, v90
	v_cvt_pkrtz_f16_f32 v16, v77, v79
	v_cvt_pkrtz_f16_f32 v17, v81, v83
	v_cvt_pkrtz_f16_f32 v18, v85, v87
	v_cvt_pkrtz_f16_f32 v19, v89, v91
	ds_write_b128 v5, v[12:15] offset:512
	ds_write_b128 v5, v[16:19] offset:2560
	s_waitcnt vmcnt(1)
	v_cvt_pkrtz_f16_f32 v12, v92, v94
	v_cvt_pkrtz_f16_f32 v13, v96, v98
	v_cvt_pkrtz_f16_f32 v14, v100, v102
	v_cvt_pkrtz_f16_f32 v15, v104, v106
	v_cvt_pkrtz_f16_f32 v16, v93, v95
	v_cvt_pkrtz_f16_f32 v17, v97, v99
	v_cvt_pkrtz_f16_f32 v18, v101, v103
	v_cvt_pkrtz_f16_f32 v19, v105, v107
	ds_write_b128 v5, v[12:15] offset:768
	ds_write_b128 v5, v[16:19] offset:2816
	s_waitcnt lgkmcnt(0)
	s_barrier
	ds_read_b128 v[12:15], v6 offset:0
	ds_read_b128 v[16:19], v6 offset:2048
	ds_read_b128 v[20:23], v7 offset:0
	ds_read_b128 v[24:27], v7 offset:2048
	ds_read_b128 v[28:31], v8 offset:0
	ds_read_b128 v[32:35], v8 offset:2048
	ds_read_b128 v[36:39], v9 offset:0
	ds_read_b128 v[40:43], v9 offset:2048
	s_waitcnt lgkmcnt(7)
	v_mfma_f32_16x16x32_f16 v[188:191], v[116:119], v[12:15], v[188:191]
	v_mfma_f32_16x16x32_f16 v[220:223], v[156:159], v[12:15], v[220:223]
	s_waitcnt lgkmcnt(6)
	v_mfma_f32_16x16x32_f16 v[192:195], v[120:123], v[16:19], v[192:195]
	v_mfma_f32_16x16x32_f16 v[224:227], v[160:163], v[16:19], v[224:227]
	s_waitcnt lgkmcnt(5)
	v_mfma_f32_16x16x32_f16 v[196:199], v[124:127], v[20:23], v[196:199]
	v_mfma_f32_16x16x32_f16 v[228:231], v[164:167], v[20:23], v[228:231]
	s_waitcnt lgkmcnt(4)
	v_mfma_f32_16x16x32_f16 v[200:203], v[128:131], v[24:27], v[200:203]
	v_mfma_f32_16x16x32_f16 v[232:235], v[168:171], v[24:27], v[232:235]
	s_waitcnt lgkmcnt(3)
	v_mfma_f32_16x16x32_f16 v[204:207], v[132:135], v[28:31], v[204:207]
	v_mfma_f32_16x16x32_f16 v[236:239], v[172:175], v[28:31], v[236:239]
	s_waitcnt lgkmcnt(2)
	v_mfma_f32_16x16x32_f16 v[208:211], v[136:139], v[32:35], v[208:211]
	v_mfma_f32_16x16x32_f16 v[240:243], v[176:179], v[32:35], v[240:243]
	s_waitcnt lgkmcnt(1)
	v_mfma_f32_16x16x32_f16 v[212:215], v[140:143], v[36:39], v[212:215]
	v_mfma_f32_16x16x32_f16 v[244:247], v[180:183], v[36:39], v[244:247]
	s_waitcnt lgkmcnt(0)
	v_mfma_f32_16x16x32_f16 v[216:219], v[144:147], v[40:43], v[216:219]
	v_mfma_f32_16x16x32_f16 v[248:251], v[184:187], v[40:43], v[248:251]
	s_nop 7
	s_nop 3
	v_and_b32_e32 v10, 1, v0
	v_cmp_eq_u32_e32 vcc, 1, v10
	s_nop 1
	v_cndmask_b32_e32 v188, v188, v220, vcc
	v_cndmask_b32_e32 v189, v189, v221, vcc
	v_cndmask_b32_e32 v190, v190, v222, vcc
	v_cndmask_b32_e32 v191, v191, v223, vcc
	v_cndmask_b32_e32 v192, v192, v224, vcc
	v_cndmask_b32_e32 v193, v193, v225, vcc
	v_cndmask_b32_e32 v194, v194, v226, vcc
	v_cndmask_b32_e32 v195, v195, v227, vcc
	v_cndmask_b32_e32 v196, v196, v228, vcc
	v_cndmask_b32_e32 v197, v197, v229, vcc
	v_cndmask_b32_e32 v198, v198, v230, vcc
	v_cndmask_b32_e32 v199, v199, v231, vcc
	v_cndmask_b32_e32 v200, v200, v232, vcc
	v_cndmask_b32_e32 v201, v201, v233, vcc
	v_cndmask_b32_e32 v202, v202, v234, vcc
	v_cndmask_b32_e32 v203, v203, v235, vcc
	v_cndmask_b32_e32 v204, v204, v236, vcc
	v_cndmask_b32_e32 v205, v205, v237, vcc
	v_cndmask_b32_e32 v206, v206, v238, vcc
	v_cndmask_b32_e32 v207, v207, v239, vcc
	v_cndmask_b32_e32 v208, v208, v240, vcc
	v_cndmask_b32_e32 v209, v209, v241, vcc
	v_cndmask_b32_e32 v210, v210, v242, vcc
	v_cndmask_b32_e32 v211, v211, v243, vcc
	v_cndmask_b32_e32 v212, v212, v244, vcc
	v_cndmask_b32_e32 v213, v213, v245, vcc
	v_cndmask_b32_e32 v214, v214, v246, vcc
	v_cndmask_b32_e32 v215, v215, v247, vcc
	v_cndmask_b32_e32 v216, v216, v248, vcc
	v_cndmask_b32_e32 v217, v217, v249, vcc
	v_cndmask_b32_e32 v218, v218, v250, vcc
	v_cndmask_b32_e32 v219, v219, v251, vcc
	s_barrier
	v_lshrrev_b32_e32 v10, 4, v2
	v_lshlrev_b32_e32 v10, 5, v10
	v_bfe_u32 v12, v2, 1, 3
	v_add_u32_e32 v10, v10, v12
	v_mul_u32_u24_e32 v10, 0x210, v10
	v_and_b32_e32 v12, 1, v2
	v_mul_u32_u24_e32 v12, 0xf8, v12
	v_add_u32_e32 v10, v10, v12
	v_lshl_add_u32 v10, v1, 5, v10
	ds_write_b32 v10, v188 offset:0
	ds_write_b32 v10, v189 offset:4224
	ds_write_b32 v10, v190 offset:8448
	ds_write_b32 v10, v191 offset:12672
	ds_write_b32 v10, v192 offset:4
	ds_write_b32 v10, v193 offset:4228
	ds_write_b32 v10, v194 offset:8452
	ds_write_b32 v10, v195 offset:12676
	s_waitcnt lgkmcnt(4)
	ds_write_b32 v10, v196 offset:8
	ds_write_b32 v10, v197 offset:4232
	ds_write_b32 v10, v198 offset:8456
	ds_write_b32 v10, v199 offset:12680
	ds_write_b32 v10, v200 offset:12
	ds_write_b32 v10, v201 offset:4236
	ds_write_b32 v10, v202 offset:8460
	ds_write_b32 v10, v203 offset:12684
	s_waitcnt lgkmcnt(4)
	ds_write_b32 v10, v204 offset:16
	ds_write_b32 v10, v205 offset:4240
	ds_write_b32 v10, v206 offset:8464
	ds_write_b32 v10, v207 offset:12688
	ds_write_b32 v10, v208 offset:20
	ds_write_b32 v10, v209 offset:4244
	ds_write_b32 v10, v210 offset:8468
	ds_write_b32 v10, v211 offset:12692
	s_waitcnt lgkmcnt(4)
	s_cmp_eq_u32 s22, 7
	s_cbranch_scc1 .Lskip_w62
	ds_write_b32 v10, v212 offset:24
	ds_write_b32 v10, v213 offset:4248
	ds_write_b32 v10, v214 offset:8472
	ds_write_b32 v10, v215 offset:12696
	ds_write_b32 v10, v216 offset:28
	ds_write_b32 v10, v217 offset:4252
	ds_write_b32 v10, v218 offset:8476
	ds_write_b32 v10, v219 offset:12700
.Lskip_w62:
	s_waitcnt lgkmcnt(0)
	s_barrier
	v_lshrrev_b32_e32 v12, 5, v0
	v_mul_u32_u24_e32 v12, 0x210, v12
	v_and_b32_e32 v13, 31, v0
	v_lshl_add_u32 v12, v13, 4, v12
	s_waitcnt vmcnt(0)
	ds_read_b128 v[108:111], v12 offset:0
	ds_read_b128 v[112:115], v12 offset:8448
	ds_read_b128 v[116:119], v12 offset:16896
	ds_read_b128 v[120:123], v12 offset:25344
	ds_read_b128 v[124:127], v12 offset:33792
	ds_read_b128 v[128:131], v12 offset:42240
	ds_read_b128 v[132:135], v12 offset:50688
	ds_read_b128 v[136:139], v12 offset:59136
	s_waitcnt lgkmcnt(7)
	v_add_f32_e32 v108, v44, v108
	v_add_f32_e32 v109, v45, v109
	v_add_f32_e32 v110, v46, v110
	v_add_f32_e32 v111, v47, v111
	s_mov_b32 s40, 0x0
	buffer_store_dwordx4 v[108:111], v11, s[32:35], s40 offen nt
	s_waitcnt lgkmcnt(6)
	v_add_f32_e32 v112, v44, v112
	v_add_f32_e32 v113, v45, v113
	v_add_f32_e32 v114, v46, v114
	v_add_f32_e32 v115, v47, v115
	s_mov_b32 s41, 0x1e0800
	buffer_store_dwordx4 v[112:115], v11, s[32:35], s41 offen nt
	s_waitcnt lgkmcnt(5)
	v_add_f32_e32 v116, v44, v116
	v_add_f32_e32 v117, v45, v117
	v_add_f32_e32 v118, v46, v118
	v_add_f32_e32 v119, v47, v119
	s_mov_b32 s42, 0x3c1000
	buffer_store_dwordx4 v[116:119], v11, s[32:35], s42 offen nt
	s_waitcnt lgkmcnt(4)
	v_add_f32_e32 v120, v44, v120
	v_add_f32_e32 v121, v45, v121
	v_add_f32_e32 v122, v46, v122
	v_add_f32_e32 v123, v47, v123
	s_mov_b32 s43, 0x5a1800
	buffer_store_dwordx4 v[120:123], v11, s[32:35], s43 offen nt
	s_waitcnt lgkmcnt(3)
	v_add_f32_e32 v124, v44, v124
	v_add_f32_e32 v125, v45, v125
	v_add_f32_e32 v126, v46, v126
	v_add_f32_e32 v127, v47, v127
	s_mov_b32 s44, 0x782000
	buffer_store_dwordx4 v[124:127], v11, s[32:35], s44 offen nt
	s_waitcnt lgkmcnt(2)
	v_add_f32_e32 v128, v44, v128
	v_add_f32_e32 v129, v45, v129
	v_add_f32_e32 v130, v46, v130
	v_add_f32_e32 v131, v47, v131
	s_mov_b32 s45, 0x962800
	buffer_store_dwordx4 v[128:131], v11, s[32:35], s45 offen nt
	s_waitcnt lgkmcnt(1)
	v_add_f32_e32 v132, v44, v132
	v_add_f32_e32 v133, v45, v133
	v_add_f32_e32 v134, v46, v134
	v_add_f32_e32 v135, v47, v135
	s_mov_b32 s46, 0xb43000
	buffer_store_dwordx4 v[132:135], v11, s[32:35], s46 offen nt
	s_waitcnt lgkmcnt(0)
	v_add_f32_e32 v136, v44, v136
	v_add_f32_e32 v137, v45, v137
	v_add_f32_e32 v138, v46, v138
	v_add_f32_e32 v139, v47, v139
	s_mov_b32 s47, 0xd23800
	buffer_store_dwordx4 v[136:139], v11, s[32:35], s47 offen nt
	s_endpgm
